# RG final pass: the eight carry-in values of a unit loaded before the step loop (were loaded in the loop right before use), selected by the loop counter
# baseline (speedup 1.0000x reference)
.LBB0_620:
	s_or_b64 exec, exec, s[4:5]
	s_waitcnt lgkmcnt(0)
	ds_read_b128 v[46:49], v94
	ds_read_b128 v[26:29], v94 offset:16
	ds_read_b128 v[42:45], v94 offset:256
	ds_read_b128 v[22:25], v94 offset:272
	ds_read_b128 v[38:41], v94 offset:512
	ds_read_b128 v[18:21], v94 offset:528
	ds_read_b128 v[34:37], v94 offset:768
	ds_read_b128 v[14:17], v94 offset:784
	s_waitcnt vmcnt(0)
	ds_read_b128 v[2:5], v106
	ds_read_b128 v[50:53], v95
	ds_read_b128 v[30:33], v95 offset:16
	ds_read_b128 v[6:9], v106 offset:144
	ds_read_b128 v[10:13], v106 offset:288
	ds_read_b128 v[54:57], v106 offset:432
	s_waitcnt lgkmcnt(5)
	v_lshlrev_b32_e32 v58, 16, v2
	v_and_b32_e32 v59, 0xffff0000, v2
	v_lshlrev_b32_e32 v2, 16, v3
	v_and_b32_e32 v3, 0xffff0000, v3
	s_waitcnt lgkmcnt(2)
	v_lshlrev_b32_e32 v60, 16, v6
	v_and_b32_e32 v61, 0xffff0000, v6
	v_pk_fma_f32 v[2:3], v[48:49], v[2:3], v[52:53]
	v_lshlrev_b32_e32 v6, 16, v7
	v_and_b32_e32 v7, 0xffff0000, v7
	v_pk_fma_f32 v[2:3], v[44:45], v[6:7], v[2:3]
	s_waitcnt lgkmcnt(1)
	v_lshlrev_b32_e32 v6, 16, v11
	v_and_b32_e32 v7, 0xffff0000, v11
	v_pk_fma_f32 v[2:3], v[40:41], v[6:7], v[2:3]
	s_waitcnt lgkmcnt(0)
	v_lshlrev_b32_e32 v6, 16, v55
	v_and_b32_e32 v7, 0xffff0000, v55
	v_pk_fma_f32 v[58:59], v[46:47], v[58:59], v[50:51]
	v_pk_fma_f32 v[6:7], v[36:37], v[6:7], v[2:3]
	v_lshlrev_b32_e32 v2, 16, v4
	v_and_b32_e32 v3, 0xffff0000, v4
	v_pk_fma_f32 v[58:59], v[42:43], v[60:61], v[58:59]
	v_lshlrev_b32_e32 v60, 16, v10
	v_and_b32_e32 v61, 0xffff0000, v10
	v_pk_fma_f32 v[2:3], v[26:27], v[2:3], v[30:31]
	v_lshlrev_b32_e32 v10, 16, v8
	v_and_b32_e32 v11, 0xffff0000, v8
	v_pk_fma_f32 v[2:3], v[22:23], v[10:11], v[2:3]
	v_lshlrev_b32_e32 v10, 16, v12
	v_and_b32_e32 v11, 0xffff0000, v12
	v_pk_fma_f32 v[2:3], v[18:19], v[10:11], v[2:3]
	v_lshlrev_b32_e32 v10, 16, v56
	v_and_b32_e32 v11, 0xffff0000, v56
	v_pk_fma_f32 v[10:11], v[14:15], v[10:11], v[2:3]
	v_lshlrev_b32_e32 v2, 16, v5
	v_and_b32_e32 v3, 0xffff0000, v5
	v_pk_fma_f32 v[2:3], v[28:29], v[2:3], v[32:33]
	v_lshlrev_b32_e32 v4, 16, v9
	v_and_b32_e32 v5, 0xffff0000, v9
	v_pk_fma_f32 v[2:3], v[24:25], v[4:5], v[2:3]
	v_lshlrev_b32_e32 v4, 16, v13
	v_and_b32_e32 v5, 0xffff0000, v13
	v_pk_fma_f32 v[2:3], v[20:21], v[4:5], v[2:3]
	v_lshlrev_b32_e32 v4, 16, v57
	v_and_b32_e32 v5, 0xffff0000, v57
	v_pk_fma_f32 v[12:13], v[16:17], v[4:5], v[2:3]
	v_cvt_pk_bf16_f32 v3, v6, v7
	ds_read_b128 v[6:9], v106 offset:2304
	v_pk_fma_f32 v[58:59], v[38:39], v[60:61], v[58:59]
	v_lshlrev_b32_e32 v60, 16, v54
	v_and_b32_e32 v61, 0xffff0000, v54
	v_pk_fma_f32 v[58:59], v[34:35], v[60:61], v[58:59]
	v_cvt_pk_bf16_f32 v4, v10, v11
	v_cvt_pk_bf16_f32 v2, v58, v59
	v_cvt_pk_bf16_f32 v5, v12, v13
	ds_read_b128 v[10:13], v106 offset:2448
	ds_read_b128 v[54:57], v106 offset:2592
	ds_read_b128 v[58:61], v106 offset:2736
	s_waitcnt lgkmcnt(3)
	v_lshlrev_b32_e32 v62, 16, v6
	v_and_b32_e32 v63, 0xffff0000, v6
	v_lshlrev_b32_e32 v6, 16, v7
	v_and_b32_e32 v7, 0xffff0000, v7
	s_waitcnt lgkmcnt(2)
	v_lshlrev_b32_e32 v64, 16, v10
	v_and_b32_e32 v65, 0xffff0000, v10
	v_pk_fma_f32 v[6:7], v[48:49], v[6:7], v[52:53]
	v_lshlrev_b32_e32 v10, 16, v11
	v_and_b32_e32 v11, 0xffff0000, v11
	v_pk_fma_f32 v[6:7], v[44:45], v[10:11], v[6:7]
	s_waitcnt lgkmcnt(1)
	v_lshlrev_b32_e32 v10, 16, v55
	v_and_b32_e32 v11, 0xffff0000, v55
	v_pk_fma_f32 v[6:7], v[40:41], v[10:11], v[6:7]
	s_waitcnt lgkmcnt(0)
	v_lshlrev_b32_e32 v10, 16, v59
	v_and_b32_e32 v11, 0xffff0000, v59
	v_pk_fma_f32 v[62:63], v[46:47], v[62:63], v[50:51]
	v_pk_fma_f32 v[10:11], v[36:37], v[10:11], v[6:7]
	v_lshlrev_b32_e32 v6, 16, v8
	v_and_b32_e32 v7, 0xffff0000, v8
	v_pk_fma_f32 v[62:63], v[42:43], v[64:65], v[62:63]
	v_lshlrev_b32_e32 v64, 16, v54
	v_and_b32_e32 v65, 0xffff0000, v54
	v_pk_fma_f32 v[6:7], v[26:27], v[6:7], v[30:31]
	v_lshlrev_b32_e32 v54, 16, v12
	v_and_b32_e32 v55, 0xffff0000, v12
	v_pk_fma_f32 v[6:7], v[22:23], v[54:55], v[6:7]
	v_lshlrev_b32_e32 v54, 16, v56
	v_and_b32_e32 v55, 0xffff0000, v56
	v_pk_fma_f32 v[6:7], v[18:19], v[54:55], v[6:7]
	v_lshlrev_b32_e32 v54, 16, v60
	v_and_b32_e32 v55, 0xffff0000, v60
	v_pk_fma_f32 v[54:55], v[14:15], v[54:55], v[6:7]
	v_lshlrev_b32_e32 v6, 16, v9
	v_and_b32_e32 v7, 0xffff0000, v9
	v_pk_fma_f32 v[6:7], v[28:29], v[6:7], v[32:33]
	v_lshlrev_b32_e32 v8, 16, v13
	v_and_b32_e32 v9, 0xffff0000, v13
	v_pk_fma_f32 v[6:7], v[24:25], v[8:9], v[6:7]
	v_lshlrev_b32_e32 v8, 16, v57
	v_and_b32_e32 v9, 0xffff0000, v57
	v_pk_fma_f32 v[6:7], v[20:21], v[8:9], v[6:7]
	v_lshlrev_b32_e32 v8, 16, v61
	v_and_b32_e32 v9, 0xffff0000, v61
	v_pk_fma_f32 v[56:57], v[16:17], v[8:9], v[6:7]
	v_cvt_pk_bf16_f32 v7, v10, v11
	ds_read_b128 v[10:13], v106 offset:4608
	v_pk_fma_f32 v[62:63], v[38:39], v[64:65], v[62:63]
	v_lshlrev_b32_e32 v64, 16, v58
	v_and_b32_e32 v65, 0xffff0000, v58
	v_pk_fma_f32 v[62:63], v[34:35], v[64:65], v[62:63]
	v_cvt_pk_bf16_f32 v8, v54, v55
	v_cvt_pk_bf16_f32 v6, v62, v63
	v_cvt_pk_bf16_f32 v9, v56, v57
	ds_read_b128 v[54:57], v106 offset:4752
	ds_read_b128 v[58:61], v106 offset:4896
	ds_read_b128 v[62:65], v106 offset:5040
	s_waitcnt lgkmcnt(3)
	v_lshlrev_b32_e32 v66, 16, v10
	v_and_b32_e32 v67, 0xffff0000, v10
	v_lshlrev_b32_e32 v10, 16, v11
	v_and_b32_e32 v11, 0xffff0000, v11
	s_waitcnt lgkmcnt(2)
	v_lshlrev_b32_e32 v68, 16, v54
	v_and_b32_e32 v69, 0xffff0000, v54
	v_pk_fma_f32 v[10:11], v[48:49], v[10:11], v[52:53]
	v_lshlrev_b32_e32 v54, 16, v55
	v_and_b32_e32 v55, 0xffff0000, v55
	v_pk_fma_f32 v[10:11], v[44:45], v[54:55], v[10:11]
	s_waitcnt lgkmcnt(1)
	v_lshlrev_b32_e32 v54, 16, v59
	v_and_b32_e32 v55, 0xffff0000, v59
	v_pk_fma_f32 v[10:11], v[40:41], v[54:55], v[10:11]
	s_waitcnt lgkmcnt(0)
	v_lshlrev_b32_e32 v54, 16, v63
	v_and_b32_e32 v55, 0xffff0000, v63
	v_pk_fma_f32 v[66:67], v[46:47], v[66:67], v[50:51]
	v_pk_fma_f32 v[54:55], v[36:37], v[54:55], v[10:11]
	v_lshlrev_b32_e32 v10, 16, v12
	v_and_b32_e32 v11, 0xffff0000, v12
	v_pk_fma_f32 v[66:67], v[42:43], v[68:69], v[66:67]
	v_lshlrev_b32_e32 v68, 16, v58
	v_and_b32_e32 v69, 0xffff0000, v58
	v_pk_fma_f32 v[10:11], v[26:27], v[10:11], v[30:31]
	v_lshlrev_b32_e32 v58, 16, v56
	v_and_b32_e32 v59, 0xffff0000, v56
	v_pk_fma_f32 v[10:11], v[22:23], v[58:59], v[10:11]
	v_lshlrev_b32_e32 v58, 16, v60
	v_and_b32_e32 v59, 0xffff0000, v60
	v_pk_fma_f32 v[10:11], v[18:19], v[58:59], v[10:11]
	v_lshlrev_b32_e32 v58, 16, v64
	v_and_b32_e32 v59, 0xffff0000, v64
	v_pk_fma_f32 v[58:59], v[14:15], v[58:59], v[10:11]
	v_lshlrev_b32_e32 v10, 16, v13
	v_and_b32_e32 v11, 0xffff0000, v13
	v_pk_fma_f32 v[10:11], v[28:29], v[10:11], v[32:33]
	v_lshlrev_b32_e32 v12, 16, v57
	v_and_b32_e32 v13, 0xffff0000, v57
	v_pk_fma_f32 v[10:11], v[24:25], v[12:13], v[10:11]
	v_lshlrev_b32_e32 v12, 16, v61
	v_and_b32_e32 v13, 0xffff0000, v61
	v_pk_fma_f32 v[10:11], v[20:21], v[12:13], v[10:11]
	v_lshlrev_b32_e32 v12, 16, v65
	v_and_b32_e32 v13, 0xffff0000, v65
	v_pk_fma_f32 v[60:61], v[16:17], v[12:13], v[10:11]
	v_cvt_pk_bf16_f32 v11, v54, v55
	ds_read_b128 v[54:57], v106 offset:6912
	v_pk_fma_f32 v[66:67], v[38:39], v[68:69], v[66:67]
	v_lshlrev_b32_e32 v68, 16, v62
	v_and_b32_e32 v69, 0xffff0000, v62
	v_pk_fma_f32 v[66:67], v[34:35], v[68:69], v[66:67]
	v_cvt_pk_bf16_f32 v12, v58, v59
	v_cvt_pk_bf16_f32 v10, v66, v67
	v_cvt_pk_bf16_f32 v13, v60, v61
	ds_read_b128 v[58:61], v106 offset:7056
	ds_read_b128 v[62:65], v106 offset:7200
	ds_read_b128 v[66:69], v106 offset:7344
	s_waitcnt lgkmcnt(3)
	v_lshlrev_b32_e32 v116, 16, v54
	v_and_b32_e32 v117, 0xffff0000, v54
	v_pk_fma_f32 v[46:47], v[46:47], v[116:117], v[50:51]
	s_waitcnt lgkmcnt(2)
	v_lshlrev_b32_e32 v50, 16, v58
	v_and_b32_e32 v51, 0xffff0000, v58
	v_pk_fma_f32 v[42:43], v[42:43], v[50:51], v[46:47]
	s_waitcnt lgkmcnt(1)
	v_lshlrev_b32_e32 v46, 16, v62
	v_and_b32_e32 v47, 0xffff0000, v62
	v_pk_fma_f32 v[38:39], v[38:39], v[46:47], v[42:43]
	s_waitcnt lgkmcnt(0)
	v_lshlrev_b32_e32 v42, 16, v66
	v_and_b32_e32 v43, 0xffff0000, v66
	v_pk_fma_f32 v[34:35], v[34:35], v[42:43], v[38:39]
	v_lshlrev_b32_e32 v38, 16, v55
	v_and_b32_e32 v39, 0xffff0000, v55
	v_pk_fma_f32 v[38:39], v[48:49], v[38:39], v[52:53]
	v_lshlrev_b32_e32 v42, 16, v59
	v_and_b32_e32 v43, 0xffff0000, v59
	v_pk_fma_f32 v[38:39], v[44:45], v[42:43], v[38:39]
	v_lshlrev_b32_e32 v42, 16, v63
	v_and_b32_e32 v43, 0xffff0000, v63
	v_pk_fma_f32 v[38:39], v[40:41], v[42:43], v[38:39]
	v_lshlrev_b32_e32 v40, 16, v67
	v_and_b32_e32 v41, 0xffff0000, v67
	v_pk_fma_f32 v[36:37], v[36:37], v[40:41], v[38:39]
	v_lshlrev_b32_e32 v38, 16, v56
	v_and_b32_e32 v39, 0xffff0000, v56
	v_pk_fma_f32 v[26:27], v[26:27], v[38:39], v[30:31]
	v_lshlrev_b32_e32 v30, 16, v60
	v_and_b32_e32 v31, 0xffff0000, v60
	v_pk_fma_f32 v[22:23], v[22:23], v[30:31], v[26:27]
	v_lshlrev_b32_e32 v26, 16, v64
	v_and_b32_e32 v27, 0xffff0000, v64
	v_pk_fma_f32 v[18:19], v[18:19], v[26:27], v[22:23]
	v_lshlrev_b32_e32 v22, 16, v68
	v_and_b32_e32 v23, 0xffff0000, v68
	v_pk_fma_f32 v[18:19], v[14:15], v[22:23], v[18:19]
	v_lshlrev_b32_e32 v14, 16, v57
	v_and_b32_e32 v15, 0xffff0000, v57
	v_pk_fma_f32 v[14:15], v[28:29], v[14:15], v[32:33]
	v_lshlrev_b32_e32 v22, 16, v61
	v_and_b32_e32 v23, 0xffff0000, v61
	v_pk_fma_f32 v[14:15], v[24:25], v[22:23], v[14:15]
	v_lshlrev_b32_e32 v22, 16, v65
	v_and_b32_e32 v23, 0xffff0000, v65
	v_pk_fma_f32 v[14:15], v[20:21], v[22:23], v[14:15]
	v_lshlrev_b32_e32 v20, 16, v69
	v_and_b32_e32 v21, 0xffff0000, v69
	v_pk_fma_f32 v[20:21], v[16:17], v[20:21], v[14:15]
	v_cvt_pk_bf16_f32 v14, v34, v35
	v_cvt_pk_bf16_f32 v15, v36, v37
	v_cvt_pk_bf16_f32 v16, v18, v19
	v_cvt_pk_bf16_f32 v17, v20, v21
	ds_read_b128 v[62:65], v96
	ds_read_b128 v[42:45], v96 offset:16
	ds_read_b128 v[58:61], v96 offset:256
	ds_read_b128 v[38:41], v96 offset:272
	ds_read_b128 v[54:57], v96 offset:512
	ds_read_b128 v[34:37], v96 offset:528
	ds_read_b128 v[50:53], v96 offset:768
	ds_read_b128 v[30:33], v96 offset:784
	ds_read_b128 v[18:21], v107
	ds_read_b128 v[66:69], v97
	ds_read_b128 v[46:49], v97 offset:16
	ds_read_b128 v[22:25], v107 offset:144
	ds_read_b128 v[26:29], v107 offset:288
	ds_read_b128 v[116:119], v107 offset:432
	s_waitcnt lgkmcnt(5)
	v_lshlrev_b32_e32 v120, 16, v18
	v_and_b32_e32 v121, 0xffff0000, v18
	v_lshlrev_b32_e32 v18, 16, v19
	v_and_b32_e32 v19, 0xffff0000, v19
	s_waitcnt lgkmcnt(2)
	v_lshlrev_b32_e32 v122, 16, v22
	v_and_b32_e32 v123, 0xffff0000, v22
	v_pk_fma_f32 v[18:19], v[64:65], v[18:19], v[68:69]
	v_lshlrev_b32_e32 v22, 16, v23
	v_and_b32_e32 v23, 0xffff0000, v23
	v_pk_fma_f32 v[18:19], v[60:61], v[22:23], v[18:19]
	s_waitcnt lgkmcnt(1)
	v_lshlrev_b32_e32 v22, 16, v27
	v_and_b32_e32 v23, 0xffff0000, v27
	v_pk_fma_f32 v[18:19], v[56:57], v[22:23], v[18:19]
	s_waitcnt lgkmcnt(0)
	v_lshlrev_b32_e32 v22, 16, v117
	v_and_b32_e32 v23, 0xffff0000, v117
	v_pk_fma_f32 v[120:121], v[62:63], v[120:121], v[66:67]
	v_pk_fma_f32 v[22:23], v[52:53], v[22:23], v[18:19]
	v_lshlrev_b32_e32 v18, 16, v20
	v_and_b32_e32 v19, 0xffff0000, v20
	v_pk_fma_f32 v[120:121], v[58:59], v[122:123], v[120:121]
	v_lshlrev_b32_e32 v122, 16, v26
	v_and_b32_e32 v123, 0xffff0000, v26
	v_pk_fma_f32 v[18:19], v[42:43], v[18:19], v[46:47]
	v_lshlrev_b32_e32 v26, 16, v24
	v_and_b32_e32 v27, 0xffff0000, v24
	v_pk_fma_f32 v[18:19], v[38:39], v[26:27], v[18:19]
	v_lshlrev_b32_e32 v26, 16, v28
	v_and_b32_e32 v27, 0xffff0000, v28
	v_pk_fma_f32 v[18:19], v[34:35], v[26:27], v[18:19]
	v_lshlrev_b32_e32 v26, 16, v118
	v_and_b32_e32 v27, 0xffff0000, v118
	v_pk_fma_f32 v[26:27], v[30:31], v[26:27], v[18:19]
	v_lshlrev_b32_e32 v18, 16, v21
	v_and_b32_e32 v19, 0xffff0000, v21
	v_pk_fma_f32 v[18:19], v[44:45], v[18:19], v[48:49]
	v_lshlrev_b32_e32 v20, 16, v25
	v_and_b32_e32 v21, 0xffff0000, v25
	v_pk_fma_f32 v[18:19], v[40:41], v[20:21], v[18:19]
	v_lshlrev_b32_e32 v20, 16, v29
	v_and_b32_e32 v21, 0xffff0000, v29
	v_pk_fma_f32 v[18:19], v[36:37], v[20:21], v[18:19]
	v_lshlrev_b32_e32 v20, 16, v119
	v_and_b32_e32 v21, 0xffff0000, v119
	v_pk_fma_f32 v[28:29], v[32:33], v[20:21], v[18:19]
	v_cvt_pk_bf16_f32 v19, v22, v23
	ds_read_b128 v[22:25], v107 offset:2304
	v_pk_fma_f32 v[120:121], v[54:55], v[122:123], v[120:121]
	v_lshlrev_b32_e32 v122, 16, v116
	v_and_b32_e32 v123, 0xffff0000, v116
	v_pk_fma_f32 v[120:121], v[50:51], v[122:123], v[120:121]
	v_cvt_pk_bf16_f32 v20, v26, v27
	v_cvt_pk_bf16_f32 v18, v120, v121
	v_cvt_pk_bf16_f32 v21, v28, v29
	ds_read_b128 v[26:29], v107 offset:2448
	ds_read_b128 v[116:119], v107 offset:2592
	ds_read_b128 v[120:123], v107 offset:2736
	s_waitcnt lgkmcnt(3)
	v_lshlrev_b32_e32 v124, 16, v22
	v_and_b32_e32 v125, 0xffff0000, v22
	v_lshlrev_b32_e32 v22, 16, v23
	v_and_b32_e32 v23, 0xffff0000, v23
	s_waitcnt lgkmcnt(2)
	v_lshlrev_b32_e32 v126, 16, v26
	v_and_b32_e32 v127, 0xffff0000, v26
	v_pk_fma_f32 v[22:23], v[64:65], v[22:23], v[68:69]
	v_lshlrev_b32_e32 v26, 16, v27
	v_and_b32_e32 v27, 0xffff0000, v27
	v_pk_fma_f32 v[22:23], v[60:61], v[26:27], v[22:23]
	s_waitcnt lgkmcnt(1)
	v_lshlrev_b32_e32 v26, 16, v117
	v_and_b32_e32 v27, 0xffff0000, v117
	v_pk_fma_f32 v[22:23], v[56:57], v[26:27], v[22:23]
	s_waitcnt lgkmcnt(0)
	v_lshlrev_b32_e32 v26, 16, v121
	v_and_b32_e32 v27, 0xffff0000, v121
	v_pk_fma_f32 v[124:125], v[62:63], v[124:125], v[66:67]
	v_pk_fma_f32 v[26:27], v[52:53], v[26:27], v[22:23]
	v_lshlrev_b32_e32 v22, 16, v24
	v_and_b32_e32 v23, 0xffff0000, v24
	v_pk_fma_f32 v[124:125], v[58:59], v[126:127], v[124:125]
	v_lshlrev_b32_e32 v126, 16, v116
	v_and_b32_e32 v127, 0xffff0000, v116
	v_pk_fma_f32 v[22:23], v[42:43], v[22:23], v[46:47]
	v_lshlrev_b32_e32 v116, 16, v28
	v_and_b32_e32 v117, 0xffff0000, v28
	v_pk_fma_f32 v[22:23], v[38:39], v[116:117], v[22:23]
	v_lshlrev_b32_e32 v116, 16, v118
	v_and_b32_e32 v117, 0xffff0000, v118
	v_pk_fma_f32 v[22:23], v[34:35], v[116:117], v[22:23]
	v_lshlrev_b32_e32 v116, 16, v122
	v_and_b32_e32 v117, 0xffff0000, v122
	v_pk_fma_f32 v[116:117], v[30:31], v[116:117], v[22:23]
	v_lshlrev_b32_e32 v22, 16, v25
	v_and_b32_e32 v23, 0xffff0000, v25
	v_pk_fma_f32 v[22:23], v[44:45], v[22:23], v[48:49]
	v_lshlrev_b32_e32 v24, 16, v29
	v_and_b32_e32 v25, 0xffff0000, v29
	v_pk_fma_f32 v[22:23], v[40:41], v[24:25], v[22:23]
	v_lshlrev_b32_e32 v24, 16, v119
	v_and_b32_e32 v25, 0xffff0000, v119
	v_pk_fma_f32 v[22:23], v[36:37], v[24:25], v[22:23]
	v_lshlrev_b32_e32 v24, 16, v123
	v_and_b32_e32 v25, 0xffff0000, v123
	v_pk_fma_f32 v[118:119], v[32:33], v[24:25], v[22:23]
	v_cvt_pk_bf16_f32 v23, v26, v27
	ds_read_b128 v[26:29], v107 offset:4608
	v_pk_fma_f32 v[124:125], v[54:55], v[126:127], v[124:125]
	v_lshlrev_b32_e32 v126, 16, v120
	v_and_b32_e32 v127, 0xffff0000, v120
	v_pk_fma_f32 v[124:125], v[50:51], v[126:127], v[124:125]
	v_cvt_pk_bf16_f32 v24, v116, v117
	v_cvt_pk_bf16_f32 v22, v124, v125
	v_cvt_pk_bf16_f32 v25, v118, v119
	ds_read_b128 v[116:119], v107 offset:4752
	ds_read_b128 v[120:123], v107 offset:4896
	ds_read_b128 v[124:127], v107 offset:5040
	s_waitcnt lgkmcnt(3)
	v_lshlrev_b32_e32 v128, 16, v26
	v_and_b32_e32 v129, 0xffff0000, v26
	v_lshlrev_b32_e32 v26, 16, v27
	v_and_b32_e32 v27, 0xffff0000, v27
	s_waitcnt lgkmcnt(2)
	v_lshlrev_b32_e32 v130, 16, v116
	v_and_b32_e32 v131, 0xffff0000, v116
	v_pk_fma_f32 v[26:27], v[64:65], v[26:27], v[68:69]
	v_lshlrev_b32_e32 v116, 16, v117
	v_and_b32_e32 v117, 0xffff0000, v117
	v_pk_fma_f32 v[26:27], v[60:61], v[116:117], v[26:27]
	s_waitcnt lgkmcnt(1)
	v_lshlrev_b32_e32 v116, 16, v121
	v_and_b32_e32 v117, 0xffff0000, v121
	v_pk_fma_f32 v[26:27], v[56:57], v[116:117], v[26:27]
	s_waitcnt lgkmcnt(0)
	v_lshlrev_b32_e32 v116, 16, v125
	v_and_b32_e32 v117, 0xffff0000, v125
	v_pk_fma_f32 v[128:129], v[62:63], v[128:129], v[66:67]
	v_pk_fma_f32 v[116:117], v[52:53], v[116:117], v[26:27]
	v_lshlrev_b32_e32 v26, 16, v28
	v_and_b32_e32 v27, 0xffff0000, v28
	v_pk_fma_f32 v[128:129], v[58:59], v[130:131], v[128:129]
	v_lshlrev_b32_e32 v130, 16, v120
	v_and_b32_e32 v131, 0xffff0000, v120
	v_pk_fma_f32 v[26:27], v[42:43], v[26:27], v[46:47]
	v_lshlrev_b32_e32 v120, 16, v118
	v_and_b32_e32 v121, 0xffff0000, v118
	v_pk_fma_f32 v[26:27], v[38:39], v[120:121], v[26:27]
	v_lshlrev_b32_e32 v120, 16, v122
	v_and_b32_e32 v121, 0xffff0000, v122
	v_pk_fma_f32 v[26:27], v[34:35], v[120:121], v[26:27]
	v_lshlrev_b32_e32 v120, 16, v126
	v_and_b32_e32 v121, 0xffff0000, v126
	v_pk_fma_f32 v[120:121], v[30:31], v[120:121], v[26:27]
	v_lshlrev_b32_e32 v26, 16, v29
	v_and_b32_e32 v27, 0xffff0000, v29
	v_pk_fma_f32 v[26:27], v[44:45], v[26:27], v[48:49]
	v_lshlrev_b32_e32 v28, 16, v119
	v_and_b32_e32 v29, 0xffff0000, v119
	v_pk_fma_f32 v[26:27], v[40:41], v[28:29], v[26:27]
	v_lshlrev_b32_e32 v28, 16, v123
	v_and_b32_e32 v29, 0xffff0000, v123
	v_pk_fma_f32 v[26:27], v[36:37], v[28:29], v[26:27]
	v_lshlrev_b32_e32 v28, 16, v127
	v_and_b32_e32 v29, 0xffff0000, v127
	v_pk_fma_f32 v[122:123], v[32:33], v[28:29], v[26:27]
	v_cvt_pk_bf16_f32 v27, v116, v117
	ds_read_b128 v[116:119], v107 offset:6912
	v_pk_fma_f32 v[128:129], v[54:55], v[130:131], v[128:129]
	v_lshlrev_b32_e32 v130, 16, v124
	v_and_b32_e32 v131, 0xffff0000, v124
	v_pk_fma_f32 v[128:129], v[50:51], v[130:131], v[128:129]
	v_cvt_pk_bf16_f32 v28, v120, v121
	v_cvt_pk_bf16_f32 v26, v128, v129
	v_cvt_pk_bf16_f32 v29, v122, v123
	ds_read_b128 v[120:123], v107 offset:7056
	ds_read_b128 v[124:127], v107 offset:7200
	ds_read_b128 v[128:131], v107 offset:7344
	s_waitcnt lgkmcnt(3)
	v_lshlrev_b32_e32 v132, 16, v116
	v_and_b32_e32 v133, 0xffff0000, v116
	v_pk_fma_f32 v[62:63], v[62:63], v[132:133], v[66:67]
	s_waitcnt lgkmcnt(2)
	v_lshlrev_b32_e32 v66, 16, v120
	v_and_b32_e32 v67, 0xffff0000, v120
	v_pk_fma_f32 v[58:59], v[58:59], v[66:67], v[62:63]
	s_waitcnt lgkmcnt(1)
	v_lshlrev_b32_e32 v62, 16, v124
	v_and_b32_e32 v63, 0xffff0000, v124
	v_pk_fma_f32 v[54:55], v[54:55], v[62:63], v[58:59]
	s_waitcnt lgkmcnt(0)
	v_lshlrev_b32_e32 v58, 16, v128
	v_and_b32_e32 v59, 0xffff0000, v128
	v_pk_fma_f32 v[50:51], v[50:51], v[58:59], v[54:55]
	v_lshlrev_b32_e32 v54, 16, v117
	v_and_b32_e32 v55, 0xffff0000, v117
	v_pk_fma_f32 v[54:55], v[64:65], v[54:55], v[68:69]
	v_lshlrev_b32_e32 v58, 16, v121
	v_and_b32_e32 v59, 0xffff0000, v121
	v_pk_fma_f32 v[54:55], v[60:61], v[58:59], v[54:55]
	v_lshlrev_b32_e32 v58, 16, v125
	v_and_b32_e32 v59, 0xffff0000, v125
	v_pk_fma_f32 v[54:55], v[56:57], v[58:59], v[54:55]
	v_lshlrev_b32_e32 v56, 16, v129
	v_and_b32_e32 v57, 0xffff0000, v129
	v_pk_fma_f32 v[52:53], v[52:53], v[56:57], v[54:55]
	v_lshlrev_b32_e32 v54, 16, v118
	v_and_b32_e32 v55, 0xffff0000, v118
	v_pk_fma_f32 v[42:43], v[42:43], v[54:55], v[46:47]
	v_lshlrev_b32_e32 v46, 16, v122
	v_and_b32_e32 v47, 0xffff0000, v122
	v_pk_fma_f32 v[38:39], v[38:39], v[46:47], v[42:43]
	v_lshlrev_b32_e32 v42, 16, v126
	v_and_b32_e32 v43, 0xffff0000, v126
	v_pk_fma_f32 v[34:35], v[34:35], v[42:43], v[38:39]
	v_lshlrev_b32_e32 v38, 16, v130
	v_and_b32_e32 v39, 0xffff0000, v130
	v_pk_fma_f32 v[34:35], v[30:31], v[38:39], v[34:35]
	v_lshlrev_b32_e32 v30, 16, v119
	v_and_b32_e32 v31, 0xffff0000, v119
	v_pk_fma_f32 v[30:31], v[44:45], v[30:31], v[48:49]
	v_lshlrev_b32_e32 v38, 16, v123
	v_and_b32_e32 v39, 0xffff0000, v123
	s_ashr_i32 s5, s16, 31
	s_mul_hi_i32 s17, s13, 0x84
	s_mulk_i32 s13, 0x84
	v_pk_fma_f32 v[30:31], v[40:41], v[38:39], v[30:31]
	v_lshlrev_b32_e32 v38, 16, v127
	v_and_b32_e32 v39, 0xffff0000, v127
	s_add_u32 s4, s13, s16
	v_pk_fma_f32 v[30:31], v[36:37], v[38:39], v[30:31]
	v_lshlrev_b32_e32 v36, 16, v131
	v_and_b32_e32 v37, 0xffff0000, v131
	s_addc_u32 s5, s17, s5
	v_pk_fma_f32 v[36:37], v[32:33], v[36:37], v[30:31]
	s_lshl_b64 s[4:5], s[4:5], 12
	v_cvt_pk_bf16_f32 v30, v50, v51
	v_cvt_pk_bf16_f32 v31, v52, v53
	v_cvt_pk_bf16_f32 v32, v34, v35
	v_cvt_pk_bf16_f32 v33, v36, v37
	v_lshl_add_u64 v[66:67], v[76:77], 0, s[4:5]
	s_mov_b64 s[4:5], 0
	s_mov_b32 s34, 0x7b300000
	s_mov_b32 s35, 0
	v_lshl_add_u64 v[202:203], v[66:67], 0, s[34:35]
	global_load_dword v194, v[202:203], off
	global_load_dword v195, v[202:203], off offset:64
	global_load_dword v196, v[202:203], off offset:128
	global_load_dword v197, v[202:203], off offset:192
	s_mov_b32 s34, 0x7b720000
	v_lshl_add_u64 v[202:203], v[66:67], 0, s[34:35]
	global_load_dword v198, v[202:203], off
	global_load_dword v199, v[202:203], off offset:64
	global_load_dword v200, v[202:203], off offset:128
	global_load_dword v201, v[202:203], off offset:192
	v_mov_b32_e32 v0, v104
	v_mov_b32_e32 v116, v103
	v_mov_b32_e32 v117, v102
.LBB0_621:
	v_add_u32_e32 v128, 0, v117
	v_add_u32_e32 v34, 0x1c200, v128
	v_add_u32_e32 v35, 0x1c300, v128
	v_add_u32_e32 v36, 0x1c400, v128
	v_add_u32_e32 v37, 0x1c500, v128
	v_add_u32_e32 v38, 0x1c600, v128
	v_add_u32_e32 v118, 0, v0
	ds_read_b32 v34, v34
	ds_read_b32 v35, v35
	ds_read_b32 v36, v36
	ds_read_b32 v37, v37
	ds_read_b32 v127, v38
	ds_read_u16 v38, v118
	ds_read_u16 v40, v118 offset:288
	ds_read_u16 v42, v118 offset:576
	ds_read_u16 v44, v118 offset:864
	ds_read_u16 v39, v118 offset:144
	ds_read_u16 v41, v118 offset:432
	ds_read_u16 v43, v118 offset:720
	v_add_u32_e32 v68, 0x1c700, v128
	ds_read_b32 v143, v68
	s_waitcnt lgkmcnt(7)
	v_lshlrev_b32_e32 v38, 16, v38
	v_add_u32_e32 v68, 0x1c900, v128
	v_fma_f32 v119, v34, v38, v127
	ds_read_u16 v38, v118 offset:2304
	ds_read_b32 v137, v68
	s_waitcnt lgkmcnt(5)
	v_lshlrev_b32_e32 v39, 16, v39
	v_lshlrev_b32_e32 v40, 16, v40
	v_fmac_f32_e32 v119, v35, v39
	v_fma_f32 v120, v34, v39, v127
	ds_read_u16 v39, v118 offset:2448
	s_waitcnt lgkmcnt(5)
	v_lshlrev_b32_e32 v41, 16, v41
	v_fmac_f32_e32 v119, v36, v40
	v_fmac_f32_e32 v120, v35, v40
	v_fma_f32 v121, v34, v40, v127
	ds_read_u16 v40, v118 offset:2592
	v_lshlrev_b32_e32 v42, 16, v42
	v_fmac_f32_e32 v119, v37, v41
	v_fmac_f32_e32 v120, v36, v41
	v_fmac_f32_e32 v121, v35, v41
	v_fma_f32 v122, v34, v41, v127
	ds_read_u16 v41, v118 offset:2736
	s_waitcnt lgkmcnt(6)
	v_lshlrev_b32_e32 v43, 16, v43
	v_fmac_f32_e32 v120, v37, v42
	v_fmac_f32_e32 v121, v36, v42
	v_fmac_f32_e32 v122, v35, v42
	ds_read_u16 v42, v118 offset:2880
	v_lshlrev_b32_e32 v44, 16, v44
	v_fmac_f32_e32 v121, v37, v43
	v_fmac_f32_e32 v122, v36, v43
	s_waitcnt lgkmcnt(5)
	v_lshlrev_b32_e32 v38, 16, v38
	ds_read_u16 v43, v118 offset:3024
	v_fmac_f32_e32 v122, v37, v44
	ds_read_u16 v44, v118 offset:3168
	v_fma_f32 v123, v34, v38, v127
	ds_read_u16 v38, v118 offset:4608
	s_waitcnt lgkmcnt(6)
	v_lshlrev_b32_e32 v39, 16, v39
	s_waitcnt lgkmcnt(5)
	v_lshlrev_b32_e32 v40, 16, v40
	v_fmac_f32_e32 v123, v35, v39
	v_fma_f32 v124, v34, v39, v127
	ds_read_u16 v39, v118 offset:4752
	s_waitcnt lgkmcnt(5)
	v_lshlrev_b32_e32 v41, 16, v41
	v_fmac_f32_e32 v123, v36, v40
	v_fmac_f32_e32 v124, v35, v40
	v_fma_f32 v125, v34, v40, v127
	ds_read_u16 v40, v118 offset:4896
	s_waitcnt lgkmcnt(5)
	v_lshlrev_b32_e32 v42, 16, v42
	v_fmac_f32_e32 v123, v37, v41
	v_fmac_f32_e32 v124, v36, v41
	v_fmac_f32_e32 v125, v35, v41
	v_fma_f32 v126, v34, v41, v127
	ds_read_u16 v41, v118 offset:5040
	s_waitcnt lgkmcnt(5)
	v_lshlrev_b32_e32 v43, 16, v43
	v_fmac_f32_e32 v124, v37, v42
	v_fmac_f32_e32 v125, v36, v42
	v_fmac_f32_e32 v126, v35, v42
	ds_read_u16 v42, v118 offset:5184
	s_waitcnt lgkmcnt(5)
	v_lshlrev_b32_e32 v44, 16, v44
	v_fmac_f32_e32 v125, v37, v43
	v_fmac_f32_e32 v126, v36, v43
	s_waitcnt lgkmcnt(4)
	v_lshlrev_b32_e32 v38, 16, v38
	ds_read_u16 v43, v118 offset:5328
	v_fmac_f32_e32 v126, v37, v44
	ds_read_u16 v44, v118 offset:5472
	v_fma_f32 v129, v34, v38, v127
	ds_read_u16 v38, v118 offset:6912
	s_waitcnt lgkmcnt(6)
	v_lshlrev_b32_e32 v39, 16, v39
	s_waitcnt lgkmcnt(5)
	v_lshlrev_b32_e32 v40, 16, v40
	v_fmac_f32_e32 v129, v35, v39
	v_fma_f32 v130, v34, v39, v127
	s_waitcnt lgkmcnt(4)
	v_lshlrev_b32_e32 v41, 16, v41
	v_fmac_f32_e32 v129, v36, v40
	v_fmac_f32_e32 v130, v35, v40
	v_fma_f32 v131, v34, v40, v127
	s_waitcnt lgkmcnt(3)
	v_lshlrev_b32_e32 v42, 16, v42
	v_fmac_f32_e32 v129, v37, v41
	v_fmac_f32_e32 v130, v36, v41
	v_fmac_f32_e32 v131, v35, v41
	v_fma_f32 v132, v34, v41, v127
	ds_read_u16 v39, v118 offset:7056
	ds_read_u16 v40, v118 offset:7200
	ds_read_u16 v41, v118 offset:7344
	s_waitcnt lgkmcnt(5)
	v_lshlrev_b32_e32 v43, 16, v43
	v_fmac_f32_e32 v130, v37, v42
	v_fmac_f32_e32 v131, v36, v42
	v_fmac_f32_e32 v132, v35, v42
	ds_read_u16 v42, v118 offset:7488
	s_waitcnt lgkmcnt(5)
	v_lshlrev_b32_e32 v44, 16, v44
	v_fmac_f32_e32 v131, v37, v43
	v_fmac_f32_e32 v132, v36, v43
	ds_read_u16 v43, v118 offset:7632
	v_fmac_f32_e32 v132, v37, v44
	ds_read_u16 v44, v118 offset:7776
	s_waitcnt lgkmcnt(6)
	v_lshlrev_b32_e32 v38, 16, v38
	s_waitcnt lgkmcnt(5)
	v_lshlrev_b32_e32 v39, 16, v39
	s_waitcnt lgkmcnt(4)
	v_lshlrev_b32_e32 v40, 16, v40
	s_waitcnt lgkmcnt(3)
	v_lshlrev_b32_e32 v41, 16, v41
	s_waitcnt lgkmcnt(2)
	v_lshlrev_b32_e32 v42, 16, v42
	v_fma_f32 v133, v34, v38, v127
	v_fma_f32 v134, v34, v39, v127
	v_fma_f32 v135, v34, v40, v127
	v_fmac_f32_e32 v127, v34, v41
	s_waitcnt lgkmcnt(1)
	v_lshlrev_b32_e32 v43, 16, v43
	v_fmac_f32_e32 v133, v35, v39
	v_fmac_f32_e32 v134, v35, v40
	v_fmac_f32_e32 v135, v35, v41
	v_fmac_f32_e32 v127, v35, v42
	v_add_u32_e32 v136, 0, v116
	s_waitcnt lgkmcnt(0)
	v_lshlrev_b32_e32 v44, 16, v44
	v_fmac_f32_e32 v133, v36, v40
	v_fmac_f32_e32 v134, v36, v41
	v_fmac_f32_e32 v135, v36, v42
	v_fmac_f32_e32 v127, v36, v43
	v_add_u32_e32 v34, 0x13200, v136
	v_fmac_f32_e32 v133, v37, v41
	v_fmac_f32_e32 v134, v37, v42
	v_fmac_f32_e32 v135, v37, v43
	v_fmac_f32_e32 v127, v37, v44
	ds_read_b128 v[34:37], v34
	v_add_u32_e32 v38, 0x13240, v136
	ds_read_b128 v[42:45], v38
	s_waitcnt lgkmcnt(1)
	v_mfma_f32_16x16x32_bf16 v[38:41], v[2:5], v[34:37], 0
	v_add_u32_e32 v50, 0x15640, v136
	ds_read_b128 v[138:141], v50
	v_add_u32_e32 v68, 0x1cb00, v128
	s_waitcnt lgkmcnt(1)
	v_mfma_f32_16x16x32_bf16 v[58:61], v[18:21], v[42:45], v[38:41]
	s_mov_b32 s13, 0x7b300000
	v_mfma_f32_16x16x32_bf16 v[38:41], v[6:9], v[34:37], 0
	v_mfma_f32_16x16x32_bf16 v[46:49], v[22:25], v[42:45], v[38:41]
	s_nop 4
	v_fmamk_f32 v58, v58, 0xbfb8aa3b, v143
	v_exp_f32_e32 v58, v58
	v_fmamk_f32 v59, v59, 0xbfb8aa3b, v143
	v_mfma_f32_16x16x32_bf16 v[38:41], v[10:13], v[34:37], 0
	v_exp_f32_e32 v59, v59
	v_add_f32_e32 v58, 1.0, v58
	v_rcp_f32_e64 v58, -v58
	v_mfma_f32_16x16x32_bf16 v[34:37], v[14:17], v[34:37], 0
	v_add_f32_e32 v59, 1.0, v59
	v_rcp_f32_e64 v59, -v59
	v_fmamk_f32 v60, v60, 0xbfb8aa3b, v143
	v_mfma_f32_16x16x32_bf16 v[38:41], v[26:29], v[42:45], v[38:41]
	v_exp_f32_e32 v60, v60
	v_fmamk_f32 v61, v61, 0xbfb8aa3b, v143
	v_exp_f32_e32 v61, v61
	v_mfma_f32_16x16x32_bf16 v[34:37], v[30:33], v[42:45], v[34:37]
	v_add_u32_e32 v42, 0x15600, v136
	ds_read_b128 v[42:45], v42
	v_add_f32_e32 v60, 1.0, v60
	s_waitcnt lgkmcnt(0)
	v_mfma_f32_16x16x32_bf16 v[50:53], v[2:5], v[42:45], 0
	v_rcp_f32_e64 v60, -v60
	v_add_f32_e32 v61, 1.0, v61
	v_rcp_f32_e64 v61, -v61
	v_mfma_f32_16x16x32_bf16 v[62:65], v[18:21], v[138:141], v[50:53]
	v_mfma_f32_16x16x32_bf16 v[50:53], v[6:9], v[42:45], 0
	v_mfma_f32_16x16x32_bf16 v[54:57], v[22:25], v[138:141], v[50:53]
	s_nop 5
	v_fmamk_f32 v62, v62, 0xbfb8aa3b, v137
	v_exp_f32_e32 v62, v62
	v_mfma_f32_16x16x32_bf16 v[50:53], v[10:13], v[42:45], 0
	v_add_f32_e32 v62, 1.0, v62
	v_rcp_f32_e32 v62, v62
	v_mfma_f32_16x16x32_bf16 v[42:45], v[14:17], v[42:45], 0
	v_mfma_f32_16x16x32_bf16 v[50:53], v[26:29], v[138:141], v[50:53]
	v_mfma_f32_16x16x32_bf16 v[42:45], v[30:33], v[138:141], v[42:45]
	ds_read_b32 v139, v68
	v_lshl_add_u64 v[68:69], v[66:67], 0, s[4:5]
	v_add_co_u32_e32 v140, vcc, s13, v68
	s_waitcnt lgkmcnt(0)
	v_mul_f32_e32 v58, v139, v58
	v_addc_co_u32_e32 v141, vcc, 0, v69, vcc
	s_waitcnt vmcnt(0)
	v_mov_b32_e32 v138, v194
	s_cmp_eq_u32 s4, 64
	s_cselect_b64 s[34:35], -1, 0
	v_cndmask_b32_e64 v138, v138, v195, s[34:35]
	s_cmp_eq_u32 s4, 0x80
	s_cselect_b64 s[34:35], -1, 0
	v_cndmask_b32_e64 v138, v138, v196, s[34:35]
	s_cmp_eq_u32 s4, 0xc0
	s_cselect_b64 s[34:35], -1, 0
	v_cndmask_b32_e64 v138, v138, v197, s[34:35]
	v_exp_f32_e32 v140, v58
	v_mul_f32_e32 v59, v139, v59
	v_exp_f32_e32 v59, v59
	v_mul_f32_e32 v60, v139, v60
	v_fma_f32 v58, -v140, v140, 1.0
	v_sqrt_f32_e32 v58, v58
	v_exp_f32_e32 v60, v60
	v_mul_f32_e32 v61, v139, v61
	v_exp_f32_e32 v61, v61
	v_mul_f32_e32 v58, v62, v58
	v_fmamk_f32 v62, v63, 0xbfb8aa3b, v137
	v_exp_f32_e32 v62, v62
	v_fma_f32 v63, -v59, v59, 1.0
	v_sqrt_f32_e32 v63, v63
	v_mul_f32_e32 v58, v119, v58
	v_add_f32_e32 v62, 1.0, v62
	v_rcp_f32_e32 v62, v62
	s_nop 0
	v_mul_f32_e32 v62, v62, v63
	v_fmamk_f32 v63, v64, 0xbfb8aa3b, v137
	v_exp_f32_e32 v63, v63
	v_fma_f32 v64, -v60, v60, 1.0
	v_sqrt_f32_e32 v64, v64
	v_add_f32_e32 v63, 1.0, v63
	v_rcp_f32_e32 v63, v63
	s_nop 0
	v_mul_f32_e32 v63, v63, v64
	v_fmamk_f32 v64, v65, 0xbfb8aa3b, v137
	v_exp_f32_e32 v64, v64
	v_fma_f32 v65, -v61, v61, 1.0
	v_sqrt_f32_e32 v65, v65
	v_add_f32_e32 v64, 1.0, v64
	v_rcp_f32_e32 v64, v64
	s_nop 0
	v_mul_f32_e32 v64, v64, v65
	v_mul_f32_e32 v65, v59, v140
	v_mul_f32_e32 v59, v59, v58
	v_fmac_f32_e32 v59, v120, v62
	v_mul_f32_e32 v141, v60, v65
	v_mul_f32_e32 v60, v60, v59
	v_fmac_f32_e32 v60, v121, v63
	v_mul_f32_e32 v142, v61, v141
	v_mul_f32_e32 v61, v61, v60
	v_fmac_f32_e32 v61, v122, v64
	ds_bpermute_b32 v62, v98, v142
	ds_bpermute_b32 v63, v98, v61
	ds_bpermute_b32 v64, v99, v142
	ds_bpermute_b32 v144, v99, v61
	ds_bpermute_b32 v145, v100, v142
	ds_bpermute_b32 v146, v100, v61
	ds_bpermute_b32 v147, v101, v142
	ds_bpermute_b32 v148, v101, v61
	s_waitcnt vmcnt(0) lgkmcnt(6)
	v_fmac_f32_e32 v63, v138, v62
	v_cndmask_b32_e64 v62, v138, v63, s[42:43]
	s_waitcnt lgkmcnt(4)
	v_fmac_f32_e32 v144, v63, v64
	v_cndmask_b32_e64 v62, v62, v144, s[44:45]
	s_waitcnt lgkmcnt(2)
	v_fmac_f32_e32 v146, v144, v145
	v_cndmask_b32_e64 v62, v62, v146, s[46:47]
	s_waitcnt lgkmcnt(0)
	v_fmac_f32_e32 v148, v146, v147
	v_fmac_f32_e32 v58, v140, v62
	v_fmac_f32_e32 v59, v65, v62
	v_fmac_f32_e32 v60, v141, v62
	v_fmac_f32_e32 v61, v142, v62
	v_fmamk_f32 v46, v46, 0xbfb8aa3b, v143
	v_exp_f32_e32 v46, v46
	v_fmamk_f32 v47, v47, 0xbfb8aa3b, v143
	v_exp_f32_e32 v47, v47
	v_fmamk_f32 v48, v48, 0xbfb8aa3b, v143
	v_add_f32_e32 v46, 1.0, v46
	v_rcp_f32_e64 v46, -v46
	v_exp_f32_e32 v48, v48
	v_fmamk_f32 v49, v49, 0xbfb8aa3b, v143
	v_exp_f32_e32 v49, v49
	v_fmamk_f32 v54, v54, 0xbfb8aa3b, v137
	v_mul_f32_e32 v46, v139, v46
	v_add_f32_e32 v47, 1.0, v47
	v_exp_f32_e32 v54, v54
	v_exp_f32_e32 v46, v46
	v_rcp_f32_e64 v47, -v47
	v_add_f32_e32 v48, 1.0, v48
	v_rcp_f32_e64 v48, -v48
	v_add_f32_e32 v49, 1.0, v49
	v_rcp_f32_e64 v49, -v49
	v_fmamk_f32 v55, v55, 0xbfb8aa3b, v137
	v_add_f32_e32 v54, 1.0, v54
	v_fma_f32 v62, -v46, v46, 1.0
	v_mul_f32_e32 v47, v139, v47
	v_rcp_f32_e32 v54, v54
	v_sqrt_f32_e32 v62, v62
	v_exp_f32_e32 v55, v55
	v_exp_f32_e32 v47, v47
	v_fmamk_f32 v56, v56, 0xbfb8aa3b, v137
	v_mul_f32_e32 v48, v139, v48
	v_exp_f32_e32 v56, v56
	v_exp_f32_e32 v48, v48
	v_fmamk_f32 v57, v57, 0xbfb8aa3b, v137
	v_mul_f32_e32 v49, v139, v49
	v_exp_f32_e32 v57, v57
	v_exp_f32_e32 v49, v49
	v_mul_f32_e32 v54, v54, v62
	v_add_f32_e32 v55, 1.0, v55
	v_fma_f32 v62, -v47, v47, 1.0
	v_rcp_f32_e32 v55, v55
	v_sqrt_f32_e32 v63, v62
	v_add_f32_e32 v56, 1.0, v56
	v_fma_f32 v62, -v48, v48, 1.0
	v_rcp_f32_e32 v56, v56
	v_sqrt_f32_e32 v64, v62
	v_add_f32_e32 v57, 1.0, v57
	v_fma_f32 v62, -v49, v49, 1.0
	v_rcp_f32_e32 v57, v57
	v_sqrt_f32_e32 v65, v62
	v_mul_f32_e32 v62, v123, v54
	v_mul_f32_e32 v54, v55, v63
	v_mul_f32_e32 v63, v47, v62
	v_fmac_f32_e32 v63, v124, v54
	v_mul_f32_e32 v55, v56, v64
	v_mul_f32_e32 v64, v48, v63
	v_mul_f32_e32 v56, v57, v65
	v_mul_f32_e32 v57, v47, v46
	v_fmac_f32_e32 v64, v125, v55
	v_mul_f32_e32 v138, v48, v57
	v_mul_f32_e32 v65, v49, v64
	v_mul_f32_e32 v140, v49, v138
	v_fmac_f32_e32 v65, v126, v56
	ds_bpermute_b32 v47, v98, v140
	ds_bpermute_b32 v48, v98, v65
	ds_bpermute_b32 v49, v99, v140
	ds_bpermute_b32 v54, v99, v65
	ds_bpermute_b32 v55, v100, v140
	ds_bpermute_b32 v56, v100, v65
	ds_bpermute_b32 v141, v101, v140
	ds_bpermute_b32 v144, v101, v65
	s_waitcnt lgkmcnt(6)
	v_fmac_f32_e32 v48, v148, v47
	v_cndmask_b32_e64 v47, v148, v48, s[42:43]
	s_waitcnt lgkmcnt(4)
	v_fmac_f32_e32 v54, v48, v49
	v_cndmask_b32_e64 v47, v47, v54, s[44:45]
	s_waitcnt lgkmcnt(2)
	v_fmac_f32_e32 v56, v54, v55
	v_cndmask_b32_e64 v47, v47, v56, s[46:47]
	s_waitcnt lgkmcnt(0)
	v_fmac_f32_e32 v144, v56, v141
	v_fmac_f32_e32 v62, v46, v47
	v_fmac_f32_e32 v63, v57, v47
	v_fmac_f32_e32 v64, v138, v47
	v_fmac_f32_e32 v65, v140, v47
	v_fmamk_f32 v38, v38, 0xbfb8aa3b, v143
	v_exp_f32_e32 v38, v38
	v_fmamk_f32 v39, v39, 0xbfb8aa3b, v143
	v_exp_f32_e32 v39, v39
	v_fmamk_f32 v40, v40, 0xbfb8aa3b, v143
	v_add_f32_e32 v38, 1.0, v38
	v_rcp_f32_e64 v38, -v38
	v_exp_f32_e32 v40, v40
	v_fmamk_f32 v41, v41, 0xbfb8aa3b, v143
	v_fmamk_f32 v46, v50, 0xbfb8aa3b, v137
	v_mul_f32_e32 v38, v139, v38
	v_add_f32_e32 v39, 1.0, v39
	v_exp_f32_e32 v41, v41
	v_exp_f32_e32 v46, v46
	v_exp_f32_e32 v38, v38
	v_rcp_f32_e64 v39, -v39
	v_add_f32_e32 v40, 1.0, v40
	v_rcp_f32_e64 v40, -v40
	v_add_f32_e32 v41, 1.0, v41
	v_fmamk_f32 v47, v51, 0xbfb8aa3b, v137
	v_add_f32_e32 v46, 1.0, v46
	v_fma_f32 v48, -v38, v38, 1.0
	v_mul_f32_e32 v39, v139, v39
	v_rcp_f32_e64 v41, -v41
	v_rcp_f32_e32 v46, v46
	v_sqrt_f32_e32 v48, v48
	v_exp_f32_e32 v47, v47
	v_exp_f32_e32 v39, v39
	v_fmamk_f32 v49, v52, 0xbfb8aa3b, v137
	v_mul_f32_e32 v40, v139, v40
	v_exp_f32_e32 v49, v49
	v_exp_f32_e32 v40, v40
	v_fmamk_f32 v51, v53, 0xbfb8aa3b, v137
	v_mul_f32_e32 v41, v139, v41
	v_mul_f32_e32 v46, v46, v48
	v_add_f32_e32 v47, 1.0, v47
	v_fma_f32 v48, -v39, v39, 1.0
	v_exp_f32_e32 v51, v51
	v_exp_f32_e32 v41, v41
	v_rcp_f32_e32 v47, v47
	v_sqrt_f32_e32 v48, v48
	v_add_f32_e32 v49, 1.0, v49
	v_fma_f32 v50, -v40, v40, 1.0
	v_rcp_f32_e32 v49, v49
	v_sqrt_f32_e32 v50, v50
	v_add_f32_e32 v51, 1.0, v51
	v_fma_f32 v52, -v41, v41, 1.0
	v_mul_f32_e32 v138, v129, v46
	v_rcp_f32_e32 v51, v51
	v_sqrt_f32_e32 v52, v52
	v_mul_f32_e32 v46, v47, v48
	v_mul_f32_e32 v140, v39, v138
	v_fmac_f32_e32 v140, v130, v46
	v_mul_f32_e32 v47, v49, v50
	v_mul_f32_e32 v141, v40, v140
	v_mul_f32_e32 v49, v39, v38
	v_fmac_f32_e32 v141, v131, v47
	v_mul_f32_e32 v48, v51, v52
	v_mul_f32_e32 v50, v40, v49
	v_mul_f32_e32 v142, v41, v141
	v_mul_f32_e32 v51, v41, v50
	v_fmac_f32_e32 v142, v132, v48
	ds_bpermute_b32 v39, v98, v51
	ds_bpermute_b32 v40, v98, v142
	ds_bpermute_b32 v41, v99, v51
	ds_bpermute_b32 v46, v99, v142
	ds_bpermute_b32 v47, v100, v51
	ds_bpermute_b32 v48, v100, v142
	ds_bpermute_b32 v52, v101, v51
	ds_bpermute_b32 v53, v101, v142
	s_waitcnt lgkmcnt(6)
	v_fmac_f32_e32 v40, v144, v39
	v_cndmask_b32_e64 v39, v144, v40, s[42:43]
	s_waitcnt lgkmcnt(4)
	v_fmac_f32_e32 v46, v40, v41
	v_cndmask_b32_e64 v39, v39, v46, s[44:45]
	s_waitcnt lgkmcnt(2)
	v_fmac_f32_e32 v48, v46, v47
	v_cndmask_b32_e64 v39, v39, v48, s[46:47]
	s_waitcnt lgkmcnt(0)
	v_fmac_f32_e32 v53, v48, v52
	v_fmac_f32_e32 v138, v38, v39
	v_fmac_f32_e32 v140, v49, v39
	v_fmac_f32_e32 v141, v50, v39
	v_fmac_f32_e32 v142, v51, v39
	v_fmamk_f32 v34, v34, 0xbfb8aa3b, v143
	v_exp_f32_e32 v34, v34
	v_fmamk_f32 v35, v35, 0xbfb8aa3b, v143
	v_exp_f32_e32 v35, v35
	v_fmamk_f32 v36, v36, 0xbfb8aa3b, v143
	v_add_f32_e32 v34, 1.0, v34
	v_rcp_f32_e64 v34, -v34
	v_exp_f32_e32 v36, v36
	v_fmac_f32_e32 v143, 0xbfb8aa3b, v37
	v_fmamk_f32 v38, v42, 0xbfb8aa3b, v137
	v_mul_f32_e32 v34, v139, v34
	v_add_f32_e32 v35, 1.0, v35
	v_exp_f32_e32 v37, v143
	v_exp_f32_e32 v38, v38
	v_exp_f32_e32 v34, v34
	v_rcp_f32_e64 v35, -v35
	v_add_f32_e32 v36, 1.0, v36
	v_rcp_f32_e64 v36, -v36
	v_add_f32_e32 v37, 1.0, v37
	v_fmamk_f32 v39, v43, 0xbfb8aa3b, v137
	v_add_f32_e32 v38, 1.0, v38
	v_fma_f32 v40, -v34, v34, 1.0
	v_mul_f32_e32 v35, v139, v35
	v_rcp_f32_e64 v37, -v37
	v_rcp_f32_e32 v38, v38
	v_sqrt_f32_e32 v40, v40
	v_exp_f32_e32 v39, v39
	v_exp_f32_e32 v35, v35
	v_fmamk_f32 v41, v44, 0xbfb8aa3b, v137
	v_mul_f32_e32 v36, v139, v36
	v_exp_f32_e32 v41, v41
	v_exp_f32_e32 v36, v36
	v_fmac_f32_e32 v137, 0xbfb8aa3b, v45
	v_mul_f32_e32 v37, v139, v37
	v_mul_f32_e32 v38, v38, v40
	v_add_f32_e32 v39, 1.0, v39
	v_fma_f32 v40, -v35, v35, 1.0
	v_exp_f32_e32 v43, v137
	v_exp_f32_e32 v37, v37
	v_rcp_f32_e32 v39, v39
	v_sqrt_f32_e32 v40, v40
	v_add_f32_e32 v41, 1.0, v41
	v_fma_f32 v42, -v36, v36, 1.0
	v_rcp_f32_e32 v41, v41
	v_sqrt_f32_e32 v42, v42
	v_add_f32_e32 v43, 1.0, v43
	v_fma_f32 v44, -v37, v37, 1.0
	v_mul_f32_e32 v139, v133, v38
	v_rcp_f32_e32 v43, v43
	v_sqrt_f32_e32 v44, v44
	v_mul_f32_e32 v38, v39, v40
	v_mul_f32_e32 v143, v35, v139
	v_fmac_f32_e32 v143, v134, v38
	v_mul_f32_e32 v39, v41, v42
	v_mul_f32_e32 v156, v36, v143
	v_mul_f32_e32 v41, v35, v34
	v_fmac_f32_e32 v156, v135, v39
	v_mul_f32_e32 v40, v43, v44
	v_mul_f32_e32 v42, v36, v41
	v_mul_f32_e32 v157, v37, v156
	v_mul_f32_e32 v43, v37, v42
	v_fmac_f32_e32 v157, v127, v40
	ds_bpermute_b32 v35, v98, v43
	ds_bpermute_b32 v36, v98, v157
	ds_bpermute_b32 v37, v99, v43
	ds_bpermute_b32 v38, v99, v157
	ds_bpermute_b32 v39, v100, v43
	ds_bpermute_b32 v40, v100, v157
	s_waitcnt lgkmcnt(4)
	v_fmac_f32_e32 v36, v53, v35
	v_cndmask_b32_e64 v35, v53, v36, s[42:43]
	s_waitcnt lgkmcnt(2)
	v_fmac_f32_e32 v38, v36, v37
	v_cndmask_b32_e64 v35, v35, v38, s[44:45]
	s_waitcnt lgkmcnt(0)
	v_fmac_f32_e32 v40, v38, v39
	v_cndmask_b32_e64 v35, v35, v40, s[46:47]
	v_fmac_f32_e32 v139, v34, v35
	v_fmac_f32_e32 v143, v41, v35
	v_fmac_f32_e32 v156, v42, v35
	v_fmac_f32_e32 v157, v43, v35
	s_mov_b32 s13, 0x7b720000
	v_add_co_u32_e32 v68, vcc, s13, v68
	v_add_u32_e32 v34, 0x17a00, v136
	v_add_u32_e32 v38, 0x17a40, v136
	v_add_u32_e32 v50, 0x19e00, v136
	v_add_u32_e32 v51, 0x19e40, v136
	v_add_u32_e32 v136, 0x1c800, v128
	v_addc_co_u32_e32 v69, vcc, 0, v69, vcc
	ds_read_b128 v[34:37], v34
	ds_read_b128 v[46:49], v38
	ds_read_b128 v[54:57], v50
	ds_read_b128 v[144:147], v51
	v_add_u32_e32 v152, 0x1ca00, v128
	v_add_u32_e32 v153, 0x1cc00, v128
	ds_read_b32 v137, v136
	ds_read_b32 v128, v152
	ds_read_b32 v136, v153
	s_waitcnt vmcnt(0)
	v_mov_b32_e32 v68, v198
	s_cmp_eq_u32 s4, 64
	s_cselect_b64 s[34:35], -1, 0
	v_cndmask_b32_e64 v68, v68, v199, s[34:35]
	s_cmp_eq_u32 s4, 0x80
	s_cselect_b64 s[34:35], -1, 0
	v_cndmask_b32_e64 v68, v68, v200, s[34:35]
	s_cmp_eq_u32 s4, 0xc0
	s_cselect_b64 s[34:35], -1, 0
	v_cndmask_b32_e64 v68, v68, v201, s[34:35]
	s_waitcnt lgkmcnt(6)
	v_mfma_f32_16x16x32_bf16 v[50:53], v[14:17], v[34:37], 0
	s_waitcnt lgkmcnt(5)
	v_mfma_f32_16x16x32_bf16 v[148:151], v[30:33], v[46:49], v[50:53]
	s_waitcnt lgkmcnt(4)
	v_mfma_f32_16x16x32_bf16 v[50:53], v[14:17], v[54:57], 0
	s_waitcnt lgkmcnt(3)
	v_mfma_f32_16x16x32_bf16 v[152:155], v[30:33], v[144:147], v[50:53]
	s_waitcnt lgkmcnt(2)
	s_nop 2
	v_fmamk_f32 v69, v148, 0xbfb8aa3b, v137
	v_fmamk_f32 v150, v150, 0xbfb8aa3b, v137
	v_exp_f32_e32 v150, v150
	v_exp_f32_e32 v50, v69
	v_mfma_f32_16x16x32_bf16 v[38:41], v[2:5], v[34:37], 0
	s_waitcnt lgkmcnt(1)
	v_fmamk_f32 v51, v152, 0xbfb8aa3b, v128
	v_exp_f32_e32 v51, v51
	v_add_f32_e32 v50, 1.0, v50
	v_rcp_f32_e64 v50, -v50
	v_mfma_f32_16x16x32_bf16 v[42:45], v[6:9], v[34:37], 0
	v_add_f32_e32 v51, 1.0, v51
	v_rcp_f32_e32 v69, v51
	s_waitcnt lgkmcnt(0)
	v_mul_f32_e32 v50, v136, v50
	v_mfma_f32_16x16x32_bf16 v[34:37], v[10:13], v[34:37], 0
	v_exp_f32_e32 v148, v50
	v_fmamk_f32 v154, v154, 0xbfb8aa3b, v128
	v_exp_f32_e32 v154, v154
	v_mfma_f32_16x16x32_bf16 v[50:53], v[26:29], v[46:49], v[34:37]
	v_mfma_f32_16x16x32_bf16 v[38:41], v[18:21], v[46:49], v[38:41]
	s_nop 2
	v_fmamk_f32 v34, v149, 0xbfb8aa3b, v137
	v_mfma_f32_16x16x32_bf16 v[42:45], v[22:25], v[46:49], v[42:45]
	v_exp_f32_e32 v46, v34
	v_fma_f32 v47, -v148, v148, 1.0
	v_sqrt_f32_e32 v149, v47
	v_fmamk_f32 v47, v153, 0xbfb8aa3b, v128
	v_add_f32_e32 v46, 1.0, v46
	v_rcp_f32_e64 v46, -v46
	v_mfma_f32_16x16x32_bf16 v[34:37], v[2:5], v[54:57], 0
	v_exp_f32_e32 v152, v47
	v_mul_f32_e32 v69, v69, v149
	v_mul_f32_e32 v153, v136, v46
	v_mfma_f32_16x16x32_bf16 v[46:49], v[6:9], v[54:57], 0
	v_exp_f32_e32 v153, v153
	v_add_f32_e32 v152, 1.0, v152
	v_rcp_f32_e32 v152, v152
	v_mfma_f32_16x16x32_bf16 v[54:57], v[10:13], v[54:57], 0
	v_fma_f32 v158, -v153, v153, 1.0
	v_sqrt_f32_e32 v158, v158
	v_mfma_f32_16x16x32_bf16 v[34:37], v[18:21], v[144:147], v[34:37]
	v_mul_f32_e32 v149, v152, v158
	v_mfma_f32_16x16x32_bf16 v[46:49], v[22:25], v[144:147], v[46:49]
	v_mfma_f32_16x16x32_bf16 v[54:57], v[26:29], v[144:147], v[54:57]
	v_fmamk_f32 v146, v151, 0xbfb8aa3b, v137
	v_exp_f32_e32 v146, v146
	v_add_f32_e32 v144, 1.0, v150
	v_rcp_f32_e64 v144, -v144
	v_fmamk_f32 v150, v155, 0xbfb8aa3b, v128
	v_add_f32_e32 v146, 1.0, v146
	v_rcp_f32_e64 v146, -v146
	v_mul_f32_e32 v144, v136, v144
	v_exp_f32_e32 v144, v144
	v_exp_f32_e32 v150, v150
	v_mul_f32_e32 v146, v136, v146
	v_exp_f32_e32 v146, v146
	v_add_f32_e32 v145, 1.0, v154
	v_fma_f32 v147, -v144, v144, 1.0
	v_add_f32_e32 v150, 1.0, v150
	v_fma_f32 v151, -v146, v146, 1.0
	v_rcp_f32_e32 v145, v145
	v_sqrt_f32_e32 v147, v147
	v_rcp_f32_e32 v150, v150
	v_sqrt_f32_e32 v151, v151
	v_mul_f32_e32 v145, v145, v147
	v_mul_f32_e32 v147, v150, v151
	v_mul_f32_e32 v147, v127, v147
	v_mul_f32_e32 v127, v144, v146
	v_mul_f32_e32 v144, v144, v147
	v_fmac_f32_e32 v144, v135, v145
	v_mul_f32_e32 v135, v153, v144
	v_fmac_f32_e32 v135, v134, v149
	v_mul_f32_e32 v150, v153, v127
	v_mul_f32_e32 v134, v148, v135
	v_mul_f32_e32 v151, v148, v150
	v_fmac_f32_e32 v134, v133, v69
	ds_bpermute_b32 v133, v101, v151
	ds_bpermute_b32 v148, v101, v134
	ds_bpermute_b32 v149, v100, v151
	ds_bpermute_b32 v152, v100, v134
	ds_bpermute_b32 v153, v99, v151
	ds_bpermute_b32 v154, v99, v134
	ds_bpermute_b32 v69, v98, v151
	ds_bpermute_b32 v145, v98, v134
	s_waitcnt vmcnt(0) lgkmcnt(6)
	v_fmac_f32_e32 v148, v68, v133
	v_cndmask_b32_e64 v68, v68, v148, s[44:45]
	s_waitcnt lgkmcnt(4)
	v_fmac_f32_e32 v152, v148, v149
	v_cndmask_b32_e64 v68, v68, v152, s[42:43]
	s_waitcnt lgkmcnt(2)
	v_fmac_f32_e32 v154, v152, v153
	v_cndmask_b32_e64 v133, v68, v154, s[40:41]
	v_fmac_f32_e32 v134, v151, v133
	v_fmac_f32_e32 v135, v150, v133
	v_fmac_f32_e32 v144, v127, v133
	v_fmac_f32_e32 v147, v146, v133
	s_waitcnt lgkmcnt(0)
	v_fmac_f32_e32 v145, v154, v69
	v_add_f32_e32 v68, v139, v134
	v_add_f32_e32 v69, v143, v135
	v_add_f32_e32 v127, v156, v144
	v_add_f32_e32 v133, v157, v147
	v_fmamk_f32 v50, v50, 0xbfb8aa3b, v137
	v_exp_f32_e32 v50, v50
	v_fmamk_f32 v51, v51, 0xbfb8aa3b, v137
	v_exp_f32_e32 v51, v51
	v_fmamk_f32 v54, v54, 0xbfb8aa3b, v128
	v_add_f32_e32 v50, 1.0, v50
	v_rcp_f32_e64 v50, -v50
	v_add_f32_e32 v51, 1.0, v51
	v_fmamk_f32 v52, v52, 0xbfb8aa3b, v137
	v_exp_f32_e32 v54, v54
	v_mul_f32_e32 v50, v136, v50
	v_exp_f32_e32 v50, v50
	v_rcp_f32_e64 v51, -v51
	v_exp_f32_e32 v52, v52
	v_add_f32_e32 v54, 1.0, v54
	v_fma_f32 v134, -v50, v50, 1.0
	v_fmamk_f32 v55, v55, 0xbfb8aa3b, v128
	v_mul_f32_e32 v51, v136, v51
	v_add_f32_e32 v52, 1.0, v52
	v_fmamk_f32 v53, v53, 0xbfb8aa3b, v137
	v_rcp_f32_e32 v54, v54
	v_sqrt_f32_e32 v134, v134
	v_exp_f32_e32 v55, v55
	v_exp_f32_e32 v51, v51
	v_rcp_f32_e64 v52, -v52
	v_exp_f32_e32 v53, v53
	v_mul_f32_e32 v54, v54, v134
	v_add_f32_e32 v55, 1.0, v55
	v_fma_f32 v134, -v51, v51, 1.0
	v_fmamk_f32 v56, v56, 0xbfb8aa3b, v128
	v_mul_f32_e32 v52, v136, v52
	v_add_f32_e32 v53, 1.0, v53
	v_rcp_f32_e32 v55, v55
	v_sqrt_f32_e32 v134, v134
	v_exp_f32_e32 v56, v56
	v_exp_f32_e32 v52, v52
	v_rcp_f32_e64 v53, -v53
	v_mul_f32_e32 v55, v55, v134
	v_add_f32_e32 v56, 1.0, v56
	v_fma_f32 v134, -v52, v52, 1.0
	v_fmamk_f32 v57, v57, 0xbfb8aa3b, v128
	v_mul_f32_e32 v53, v136, v53
	v_rcp_f32_e32 v56, v56
	v_sqrt_f32_e32 v134, v134
	v_exp_f32_e32 v57, v57
	v_exp_f32_e32 v53, v53
	v_mul_f32_e32 v56, v56, v134
	v_add_f32_e32 v57, 1.0, v57
	v_fma_f32 v134, -v53, v53, 1.0
	v_rcp_f32_e32 v57, v57
	v_sqrt_f32_e32 v134, v134
	s_nop 0
	v_mul_f32_e32 v57, v57, v134
	v_mul_f32_e32 v57, v132, v57
	v_mul_f32_e32 v132, v52, v53
	v_mul_f32_e32 v52, v52, v57
	v_fmac_f32_e32 v52, v131, v56
	v_mul_f32_e32 v134, v51, v132
	v_mul_f32_e32 v51, v51, v52
	v_fmac_f32_e32 v51, v130, v55
	v_mul_f32_e32 v135, v50, v134
	v_mul_f32_e32 v50, v50, v51
	v_fmac_f32_e32 v50, v129, v54
	ds_bpermute_b32 v139, v101, v135
	ds_bpermute_b32 v143, v101, v50
	ds_bpermute_b32 v130, v100, v135
	ds_bpermute_b32 v131, v100, v50
	ds_bpermute_b32 v56, v99, v135
	ds_bpermute_b32 v129, v99, v50
	ds_bpermute_b32 v54, v98, v135
	ds_bpermute_b32 v55, v98, v50
	s_waitcnt lgkmcnt(6)
	v_fmac_f32_e32 v143, v145, v139
	v_cndmask_b32_e64 v139, v145, v143, s[44:45]
	s_waitcnt lgkmcnt(4)
	v_fmac_f32_e32 v131, v143, v130
	v_cndmask_b32_e64 v130, v139, v131, s[42:43]
	s_waitcnt lgkmcnt(2)
	v_fmac_f32_e32 v129, v131, v56
	v_cndmask_b32_e64 v56, v130, v129, s[40:41]
	v_fmac_f32_e32 v50, v135, v56
	v_fmac_f32_e32 v51, v134, v56
	v_fmac_f32_e32 v52, v132, v56
	v_fmac_f32_e32 v57, v53, v56
	s_waitcnt lgkmcnt(0)
	v_fmac_f32_e32 v55, v129, v54
	v_add_f32_e32 v50, v138, v50
	v_add_f32_e32 v51, v140, v51
	v_add_f32_e32 v52, v141, v52
	v_add_f32_e32 v53, v142, v57
	v_fmamk_f32 v42, v42, 0xbfb8aa3b, v137
	v_exp_f32_e32 v42, v42
	v_fmamk_f32 v43, v43, 0xbfb8aa3b, v137
	v_exp_f32_e32 v43, v43
	v_fmamk_f32 v46, v46, 0xbfb8aa3b, v128
	v_add_f32_e32 v42, 1.0, v42
	v_rcp_f32_e64 v42, -v42
	v_add_f32_e32 v43, 1.0, v43
	v_fmamk_f32 v44, v44, 0xbfb8aa3b, v137
	v_exp_f32_e32 v46, v46
	v_mul_f32_e32 v42, v136, v42
	v_exp_f32_e32 v42, v42
	v_rcp_f32_e64 v43, -v43
	v_exp_f32_e32 v44, v44
	v_add_f32_e32 v46, 1.0, v46
	v_fma_f32 v54, -v42, v42, 1.0
	v_fmamk_f32 v47, v47, 0xbfb8aa3b, v128
	v_mul_f32_e32 v43, v136, v43
	v_add_f32_e32 v44, 1.0, v44
	v_fmamk_f32 v45, v45, 0xbfb8aa3b, v137
	v_rcp_f32_e32 v46, v46
	v_sqrt_f32_e32 v54, v54
	v_exp_f32_e32 v47, v47
	v_exp_f32_e32 v43, v43
	v_rcp_f32_e64 v44, -v44
	v_exp_f32_e32 v45, v45
	v_mul_f32_e32 v46, v46, v54
	v_add_f32_e32 v47, 1.0, v47
	v_fma_f32 v54, -v43, v43, 1.0
	v_fmamk_f32 v48, v48, 0xbfb8aa3b, v128
	v_mul_f32_e32 v44, v136, v44
	v_add_f32_e32 v45, 1.0, v45
	v_rcp_f32_e32 v47, v47
	v_sqrt_f32_e32 v54, v54
	v_exp_f32_e32 v48, v48
	v_exp_f32_e32 v44, v44
	v_rcp_f32_e64 v45, -v45
	v_mul_f32_e32 v47, v47, v54
	v_add_f32_e32 v48, 1.0, v48
	v_fma_f32 v54, -v44, v44, 1.0
	v_fmamk_f32 v49, v49, 0xbfb8aa3b, v128
	v_mul_f32_e32 v45, v136, v45
	v_rcp_f32_e32 v48, v48
	v_sqrt_f32_e32 v54, v54
	v_exp_f32_e32 v49, v49
	v_exp_f32_e32 v45, v45
	v_mul_f32_e32 v48, v48, v54
	v_add_f32_e32 v49, 1.0, v49
	v_fma_f32 v54, -v45, v45, 1.0
	v_rcp_f32_e32 v49, v49
	v_sqrt_f32_e32 v54, v54
	s_nop 0
	v_mul_f32_e32 v49, v49, v54
	v_mul_f32_e32 v49, v126, v49
	v_mul_f32_e32 v54, v44, v45
	v_mul_f32_e32 v44, v44, v49
	v_fmac_f32_e32 v44, v125, v48
	v_mul_f32_e32 v56, v43, v54
	v_mul_f32_e32 v43, v43, v44
	v_fmac_f32_e32 v43, v124, v47
	v_mul_f32_e32 v57, v42, v56
	v_mul_f32_e32 v42, v42, v43
	v_fmac_f32_e32 v42, v123, v46
	ds_bpermute_b32 v126, v101, v57
	ds_bpermute_b32 v129, v101, v42
	ds_bpermute_b32 v124, v100, v57
	ds_bpermute_b32 v125, v100, v42
	ds_bpermute_b32 v48, v99, v57
	ds_bpermute_b32 v123, v99, v42
	ds_bpermute_b32 v46, v98, v57
	ds_bpermute_b32 v47, v98, v42
	s_waitcnt lgkmcnt(6)
	v_fmac_f32_e32 v129, v55, v126
	v_cndmask_b32_e64 v55, v55, v129, s[44:45]
	s_waitcnt lgkmcnt(4)
	v_fmac_f32_e32 v125, v129, v124
	v_cndmask_b32_e64 v55, v55, v125, s[42:43]
	s_waitcnt lgkmcnt(2)
	v_fmac_f32_e32 v123, v125, v48
	v_cndmask_b32_e64 v48, v55, v123, s[40:41]
	v_fmac_f32_e32 v42, v57, v48
	v_fmac_f32_e32 v43, v56, v48
	v_fmac_f32_e32 v44, v54, v48
	v_fmac_f32_e32 v49, v45, v48
	s_waitcnt lgkmcnt(0)
	v_fmac_f32_e32 v47, v123, v46
	v_add_f32_e32 v42, v62, v42
	v_add_f32_e32 v43, v63, v43
	v_add_f32_e32 v44, v64, v44
	v_add_f32_e32 v45, v65, v49
	v_fmamk_f32 v38, v38, 0xbfb8aa3b, v137
	v_exp_f32_e32 v38, v38
	v_fmamk_f32 v39, v39, 0xbfb8aa3b, v137
	v_exp_f32_e32 v39, v39
	v_fmamk_f32 v40, v40, 0xbfb8aa3b, v137
	v_add_f32_e32 v38, 1.0, v38
	v_rcp_f32_e64 v38, -v38
	v_add_f32_e32 v39, 1.0, v39
	v_fmamk_f32 v34, v34, 0xbfb8aa3b, v128
	v_rcp_f32_e64 v39, -v39
	v_mul_f32_e32 v38, v136, v38
	v_exp_f32_e32 v38, v38
	v_exp_f32_e32 v40, v40
	v_exp_f32_e32 v34, v34
	v_mul_f32_e32 v39, v136, v39
	v_fmac_f32_e32 v137, 0xbfb8aa3b, v41
	v_add_f32_e32 v40, 1.0, v40
	v_add_f32_e32 v34, 1.0, v34
	v_fma_f32 v54, -v38, v38, 1.0
	v_fmamk_f32 v35, v35, 0xbfb8aa3b, v128
	v_exp_f32_e32 v39, v39
	v_rcp_f32_e64 v40, -v40
	v_exp_f32_e32 v41, v137
	v_rcp_f32_e32 v34, v34
	v_sqrt_f32_e32 v54, v54
	v_exp_f32_e32 v35, v35
	v_mul_f32_e32 v40, v136, v40
	v_add_f32_e32 v41, 1.0, v41
	v_mul_f32_e32 v34, v34, v54
	v_add_f32_e32 v35, 1.0, v35
	v_fma_f32 v54, -v39, v39, 1.0
	v_fmamk_f32 v36, v36, 0xbfb8aa3b, v128
	v_exp_f32_e32 v40, v40
	v_rcp_f32_e64 v41, -v41
	v_rcp_f32_e32 v35, v35
	v_sqrt_f32_e32 v54, v54
	v_exp_f32_e32 v36, v36
	v_mul_f32_e32 v41, v136, v41
	v_fmac_f32_e32 v128, 0xbfb8aa3b, v37
	v_mul_f32_e32 v35, v35, v54
	v_add_f32_e32 v36, 1.0, v36
	v_fma_f32 v54, -v40, v40, 1.0
	v_exp_f32_e32 v41, v41
	v_rcp_f32_e32 v36, v36
	v_sqrt_f32_e32 v54, v54
	v_exp_f32_e32 v37, v128
	v_mul_f32_e32 v46, v40, v41
	v_mul_f32_e32 v48, v39, v46
	v_mul_f32_e32 v36, v36, v54
	v_add_f32_e32 v37, 1.0, v37
	v_fma_f32 v54, -v41, v41, 1.0
	v_rcp_f32_e32 v37, v37
	v_sqrt_f32_e32 v54, v54
	v_mul_f32_e32 v49, v38, v48
	ds_bpermute_b32 v55, v101, v49
	v_mul_f32_e32 v37, v37, v54
	v_mul_f32_e32 v37, v122, v37
	v_mul_f32_e32 v40, v40, v37
	v_fmac_f32_e32 v40, v121, v36
	v_mul_f32_e32 v36, v39, v40
	v_fmac_f32_e32 v36, v120, v35
	v_mul_f32_e32 v35, v38, v36
	v_fmac_f32_e32 v35, v119, v34
	ds_bpermute_b32 v56, v101, v35
	ds_bpermute_b32 v39, v100, v49
	ds_bpermute_b32 v54, v100, v35
	ds_bpermute_b32 v34, v99, v49
	ds_bpermute_b32 v38, v99, v35
	s_waitcnt lgkmcnt(4)
	v_fmac_f32_e32 v56, v47, v55
	v_cndmask_b32_e64 v47, v47, v56, s[44:45]
	s_waitcnt lgkmcnt(2)
	v_fmac_f32_e32 v54, v56, v39
	v_cndmask_b32_e64 v39, v47, v54, s[42:43]
	s_waitcnt lgkmcnt(0)
	v_fmac_f32_e32 v38, v54, v34
	v_cndmask_b32_e64 v34, v39, v38, s[40:41]
	v_fmac_f32_e32 v35, v49, v34
	v_fmac_f32_e32 v36, v48, v34
	v_fmac_f32_e32 v40, v46, v34
	v_fmac_f32_e32 v37, v41, v34
	v_add_f32_e32 v35, v58, v35
	v_add_f32_e32 v36, v59, v36
	v_add_f32_e32 v38, v60, v40
	v_add_f32_e32 v34, v61, v37
	v_cvt_pk_bf16_f32 v34, v34, s0
	ds_write_b16 v118, v34 offset:720
	v_cvt_pk_bf16_f32 v34, v42, s0
	ds_write_b16 v118, v34 offset:2592
	v_cvt_pk_bf16_f32 v34, v43, s0
	ds_write_b16 v118, v34 offset:2736
	v_cvt_pk_bf16_f32 v34, v44, s0
	ds_write_b16 v118, v34 offset:2880
	v_cvt_pk_bf16_f32 v34, v45, s0
	ds_write_b16 v118, v34 offset:3024
	v_cvt_pk_bf16_f32 v34, v50, s0
	ds_write_b16 v118, v34 offset:4896
	v_cvt_pk_bf16_f32 v34, v51, s0
	ds_write_b16 v118, v34 offset:5040
	v_cvt_pk_bf16_f32 v34, v52, s0
	ds_write_b16 v118, v34 offset:5184
	v_cvt_pk_bf16_f32 v34, v53, s0
	ds_write_b16 v118, v34 offset:5328
	v_cvt_pk_bf16_f32 v34, v68, s0
	v_cvt_pk_bf16_f32 v35, v35, s0
	ds_write_b16 v118, v34 offset:7200
	v_cvt_pk_bf16_f32 v34, v69, s0
	s_add_u32 s4, s4, 64
	ds_write_b16 v118, v35 offset:288
	v_cvt_pk_bf16_f32 v35, v36, s0
	ds_write_b16 v118, v34 offset:7344
	v_cvt_pk_bf16_f32 v34, v127, s0
	s_addc_u32 s5, s5, 0
	ds_write_b16 v118, v35 offset:432
	v_cvt_pk_bf16_f32 v35, v38, s0
	ds_write_b16 v118, v34 offset:7488
	v_cvt_pk_bf16_f32 v34, v133, s0
	v_add_u32_e32 v117, 64, v117
	v_add_u32_e32 v116, 0x900, v116
	s_cmpk_lg_i32 s4, 0x100
	v_add_u32_e32 v0, 32, v0
	ds_write_b16 v118, v35 offset:576
	ds_write_b16 v118, v34 offset:7632
	s_cbranch_scc1 .LBB0_621
	s_add_i32 s4, s9, s8
	v_or_b32_e32 v0, s4, v71
	s_movk_i32 s13, 0x2c00
	s_waitcnt lgkmcnt(0)
	v_or_b32_e32 v48, s4, v71
	v_mad_i64_i32 v[16:17], s[8:9], v48, s13, v[74:75]
	global_load_dwordx4 v[16:19], v[16:17], off offset:3072
	v_or_b32_e32 v48, s4, v79
	v_mad_i64_i32 v[20:21], s[8:9], v48, s13, v[74:75]
	global_load_dwordx4 v[20:23], v[20:21], off offset:3072
	v_or_b32_e32 v48, s4, v81
	v_mad_i64_i32 v[24:25], s[8:9], v48, s13, v[74:75]
	global_load_dwordx4 v[24:27], v[24:25], off offset:3072
	v_or_b32_e32 v48, s4, v83
	v_mad_i64_i32 v[28:29], s[8:9], v48, s13, v[74:75]
	global_load_dwordx4 v[28:31], v[28:29], off offset:3072
	v_or_b32_e32 v48, s4, v85
	v_mad_i64_i32 v[32:33], s[8:9], v48, s13, v[74:75]
	global_load_dwordx4 v[32:35], v[32:33], off offset:3072
	v_or_b32_e32 v48, s4, v87
	v_mad_i64_i32 v[36:37], s[8:9], v48, s13, v[74:75]
	global_load_dwordx4 v[36:39], v[36:37], off offset:3072
	v_or_b32_e32 v48, s4, v89
	v_mad_i64_i32 v[40:41], s[8:9], v48, s13, v[74:75]
	global_load_dwordx4 v[40:43], v[40:41], off offset:3072
	v_or_b32_e32 v48, s4, v91
	v_mad_i64_i32 v[44:45], s[8:9], v48, s13, v[74:75]
	global_load_dwordx4 v[44:47], v[44:45], off offset:3072
	v_mad_i64_i32 v[6:7], s[8:9], v0, s13, v[74:75]
	ds_read_b128 v[2:5], v108 offset:288
	s_add_i32 s11, s11, s30
	s_cmp_lt_i32 s11, s10
	s_waitcnt lgkmcnt(0)
	v_lshlrev_b32_e32 v10, 16, v2
	v_and_b32_e32 v11, 0xffff0000, v2
	s_waitcnt vmcnt(7)
	v_mov_b32_e32 v6, v16
	v_mov_b32_e32 v7, v17
	v_mov_b32_e32 v8, v18
	v_mov_b32_e32 v9, v19
	v_lshlrev_b32_e32 v12, 16, v6
	v_mul_f32_e32 v2, 0x3d372713, v12
	v_and_b32_e32 v13, 0xffff0000, v6
	v_mul_f32_e32 v2, v2, v12
	v_mov_b32_e32 v6, v12
	v_fmac_f32_e32 v6, v2, v6
	v_mul_f32_e32 v2, 0x3f4c422a, v6
	v_add_f32_e32 v2, v2, v2
	v_mul_f32_e32 v2, 0xbfb8aa3b, v2
	v_exp_f32_e32 v2, v2
	v_mov_b32_e32 v6, v13
	v_add_f32_e32 v2, 1.0, v2
	v_rcp_f32_e32 v14, v2
	v_mul_f32_e32 v2, 0x3d372713, v13
	v_mul_f32_e32 v2, v2, v13
	v_fmac_f32_e32 v6, v2, v6
	v_mul_f32_e32 v2, 0x3f4c422a, v6
	v_add_f32_e32 v2, v2, v2
	v_mul_f32_e32 v2, 0xbfb8aa3b, v2
	v_exp_f32_e32 v2, v2
	v_lshlrev_b32_e32 v6, 16, v7
	v_and_b32_e32 v7, 0xffff0000, v7
	v_add_f32_e32 v2, 1.0, v2
	v_rcp_f32_e32 v15, v2
	s_nop 0
	v_pk_mul_f32 v[12:13], v[14:15], v[12:13]
	s_nop 0
	v_pk_mul_f32 v[10:11], v[12:13], v[10:11]
	v_mov_b32_e32 v12, v6
	v_cvt_pk_bf16_f32 v2, v10, v11
	v_lshlrev_b32_e32 v10, 16, v3
	v_and_b32_e32 v11, 0xffff0000, v3
	v_mul_f32_e32 v3, 0x3d372713, v6
	v_mul_f32_e32 v3, v3, v6
	v_fmac_f32_e32 v12, v3, v12
	v_mul_f32_e32 v3, 0x3f4c422a, v12
	v_add_f32_e32 v3, v3, v3
	v_mul_f32_e32 v3, 0xbfb8aa3b, v3
	v_exp_f32_e32 v3, v3
	v_mov_b32_e32 v13, v7
	v_add_f32_e32 v3, 1.0, v3
	v_rcp_f32_e32 v12, v3
	v_mul_f32_e32 v3, 0x3d372713, v7
	v_mul_f32_e32 v3, v3, v7
	v_fmac_f32_e32 v13, v3, v13
	v_mul_f32_e32 v3, 0x3f4c422a, v13
	v_add_f32_e32 v3, v3, v3
	v_mul_f32_e32 v3, 0xbfb8aa3b, v3
	v_exp_f32_e32 v3, v3
	s_nop 0
	v_add_f32_e32 v3, 1.0, v3
	v_rcp_f32_e32 v13, v3
	s_nop 0
	v_pk_mul_f32 v[6:7], v[12:13], v[6:7]
	s_nop 0
	v_pk_mul_f32 v[6:7], v[6:7], v[10:11]
	v_lshlrev_b32_e32 v10, 16, v8
	v_cvt_pk_bf16_f32 v3, v6, v7
	v_lshlrev_b32_e32 v6, 16, v4
	v_and_b32_e32 v7, 0xffff0000, v4
	v_mul_f32_e32 v4, 0x3d372713, v10
	v_and_b32_e32 v11, 0xffff0000, v8
	v_mul_f32_e32 v4, v4, v10
	v_mov_b32_e32 v8, v10
	v_fmac_f32_e32 v8, v4, v8
	v_mul_f32_e32 v4, 0x3f4c422a, v8
	v_add_f32_e32 v4, v4, v4
	v_mul_f32_e32 v4, 0xbfb8aa3b, v4
	v_exp_f32_e32 v4, v4
	v_mov_b32_e32 v8, v11
	v_add_f32_e32 v4, 1.0, v4
	v_rcp_f32_e32 v12, v4
	v_mul_f32_e32 v4, 0x3d372713, v11
	v_mul_f32_e32 v4, v4, v11
	v_fmac_f32_e32 v8, v4, v8
	v_mul_f32_e32 v4, 0x3f4c422a, v8
	v_add_f32_e32 v4, v4, v4
	v_mul_f32_e32 v4, 0xbfb8aa3b, v4
	v_exp_f32_e32 v4, v4
	v_lshlrev_b32_e32 v8, 16, v9
	v_and_b32_e32 v9, 0xffff0000, v9
	v_add_f32_e32 v4, 1.0, v4
	v_rcp_f32_e32 v13, v4
	s_nop 0
	v_pk_mul_f32 v[10:11], v[12:13], v[10:11]
	s_nop 0
	v_pk_mul_f32 v[6:7], v[10:11], v[6:7]
	v_mov_b32_e32 v10, v8
	v_cvt_pk_bf16_f32 v4, v6, v7
	v_lshlrev_b32_e32 v6, 16, v5
	v_and_b32_e32 v7, 0xffff0000, v5
	v_mul_f32_e32 v5, 0x3d372713, v8
	v_mul_f32_e32 v5, v5, v8
	v_fmac_f32_e32 v10, v5, v10
	v_mul_f32_e32 v5, 0x3f4c422a, v10
	v_add_f32_e32 v5, v5, v5
	v_mul_f32_e32 v5, 0xbfb8aa3b, v5
	v_exp_f32_e32 v5, v5
	v_mov_b32_e32 v11, v9
	v_add_f32_e32 v5, 1.0, v5
	v_rcp_f32_e32 v10, v5
	v_mul_f32_e32 v5, 0x3d372713, v9
	v_mul_f32_e32 v5, v5, v9
	v_fmac_f32_e32 v11, v5, v11
	v_mul_f32_e32 v5, 0x3f4c422a, v11
	v_add_f32_e32 v5, v5, v5
	v_mul_f32_e32 v5, 0xbfb8aa3b, v5
	v_exp_f32_e32 v5, v5
	s_nop 0
	v_add_f32_e32 v5, 1.0, v5
	v_rcp_f32_e32 v11, v5
	s_nop 0
	v_pk_mul_f32 v[8:9], v[10:11], v[8:9]
	s_nop 0
	v_pk_mul_f32 v[6:7], v[8:9], v[6:7]
	s_nop 0
	v_cvt_pk_bf16_f32 v5, v6, v7
	v_mad_i64_i32 v[6:7], s[8:9], v0, s13, v[72:73]
	v_or_b32_e32 v0, s4, v79
	global_store_dwordx4 v[6:7], v[2:5], off
	v_mad_i64_i32 v[6:7], s[8:9], v0, s13, v[74:75]
	ds_read_b128 v[2:5], v109 offset:288
	s_waitcnt lgkmcnt(0)
	v_lshlrev_b32_e32 v10, 16, v2
	v_and_b32_e32 v11, 0xffff0000, v2
	s_waitcnt vmcnt(7)
	v_mov_b32_e32 v6, v20
	v_mov_b32_e32 v7, v21
	v_mov_b32_e32 v8, v22
	v_mov_b32_e32 v9, v23
	v_lshlrev_b32_e32 v12, 16, v6
	v_mul_f32_e32 v2, 0x3d372713, v12
	v_and_b32_e32 v13, 0xffff0000, v6
	v_mul_f32_e32 v2, v2, v12
	v_mov_b32_e32 v6, v12
	v_fmac_f32_e32 v6, v2, v6
	v_mul_f32_e32 v2, 0x3f4c422a, v6
	v_add_f32_e32 v2, v2, v2
	v_mul_f32_e32 v2, 0xbfb8aa3b, v2
	v_exp_f32_e32 v2, v2
	v_mov_b32_e32 v6, v13
	v_add_f32_e32 v2, 1.0, v2
	v_rcp_f32_e32 v14, v2
	v_mul_f32_e32 v2, 0x3d372713, v13
	v_mul_f32_e32 v2, v2, v13
	v_fmac_f32_e32 v6, v2, v6
	v_mul_f32_e32 v2, 0x3f4c422a, v6
	v_add_f32_e32 v2, v2, v2
	v_mul_f32_e32 v2, 0xbfb8aa3b, v2
	v_exp_f32_e32 v2, v2
	v_lshlrev_b32_e32 v6, 16, v7
	v_and_b32_e32 v7, 0xffff0000, v7
	v_add_f32_e32 v2, 1.0, v2
	v_rcp_f32_e32 v15, v2
	s_nop 0
	v_pk_mul_f32 v[12:13], v[14:15], v[12:13]
	s_nop 0
	v_pk_mul_f32 v[10:11], v[12:13], v[10:11]
	v_mov_b32_e32 v12, v6
	v_cvt_pk_bf16_f32 v2, v10, v11
	v_lshlrev_b32_e32 v10, 16, v3
	v_and_b32_e32 v11, 0xffff0000, v3
	v_mul_f32_e32 v3, 0x3d372713, v6
	v_mul_f32_e32 v3, v3, v6
	v_fmac_f32_e32 v12, v3, v12
	v_mul_f32_e32 v3, 0x3f4c422a, v12
	v_add_f32_e32 v3, v3, v3
	v_mul_f32_e32 v3, 0xbfb8aa3b, v3
	v_exp_f32_e32 v3, v3
	v_mov_b32_e32 v13, v7
	v_add_f32_e32 v3, 1.0, v3
	v_rcp_f32_e32 v12, v3
	v_mul_f32_e32 v3, 0x3d372713, v7
	v_mul_f32_e32 v3, v3, v7
	v_fmac_f32_e32 v13, v3, v13
	v_mul_f32_e32 v3, 0x3f4c422a, v13
	v_add_f32_e32 v3, v3, v3
	v_mul_f32_e32 v3, 0xbfb8aa3b, v3
	v_exp_f32_e32 v3, v3
	s_nop 0
	v_add_f32_e32 v3, 1.0, v3
	v_rcp_f32_e32 v13, v3
	s_nop 0
	v_pk_mul_f32 v[6:7], v[12:13], v[6:7]
	s_nop 0
	v_pk_mul_f32 v[6:7], v[6:7], v[10:11]
	v_lshlrev_b32_e32 v10, 16, v8
	v_cvt_pk_bf16_f32 v3, v6, v7
	v_lshlrev_b32_e32 v6, 16, v4
	v_and_b32_e32 v7, 0xffff0000, v4
	v_mul_f32_e32 v4, 0x3d372713, v10
	v_and_b32_e32 v11, 0xffff0000, v8
	v_mul_f32_e32 v4, v4, v10
	v_mov_b32_e32 v8, v10
	v_fmac_f32_e32 v8, v4, v8
	v_mul_f32_e32 v4, 0x3f4c422a, v8
	v_add_f32_e32 v4, v4, v4
	v_mul_f32_e32 v4, 0xbfb8aa3b, v4
	v_exp_f32_e32 v4, v4
	v_mov_b32_e32 v8, v11
	v_add_f32_e32 v4, 1.0, v4
	v_rcp_f32_e32 v12, v4
	v_mul_f32_e32 v4, 0x3d372713, v11
	v_mul_f32_e32 v4, v4, v11
	v_fmac_f32_e32 v8, v4, v8
	v_mul_f32_e32 v4, 0x3f4c422a, v8
	v_add_f32_e32 v4, v4, v4
	v_mul_f32_e32 v4, 0xbfb8aa3b, v4
	v_exp_f32_e32 v4, v4
	v_lshlrev_b32_e32 v8, 16, v9
	v_and_b32_e32 v9, 0xffff0000, v9
	v_add_f32_e32 v4, 1.0, v4
	v_rcp_f32_e32 v13, v4
	s_nop 0
	v_pk_mul_f32 v[10:11], v[12:13], v[10:11]
	s_nop 0
	v_pk_mul_f32 v[6:7], v[10:11], v[6:7]
	v_mov_b32_e32 v10, v8
	v_cvt_pk_bf16_f32 v4, v6, v7
	v_lshlrev_b32_e32 v6, 16, v5
	v_and_b32_e32 v7, 0xffff0000, v5
	v_mul_f32_e32 v5, 0x3d372713, v8
	v_mul_f32_e32 v5, v5, v8
	v_fmac_f32_e32 v10, v5, v10
	v_mul_f32_e32 v5, 0x3f4c422a, v10
	v_add_f32_e32 v5, v5, v5
	v_mul_f32_e32 v5, 0xbfb8aa3b, v5
	v_exp_f32_e32 v5, v5
	v_mov_b32_e32 v11, v9
	v_add_f32_e32 v5, 1.0, v5
	v_rcp_f32_e32 v10, v5
	v_mul_f32_e32 v5, 0x3d372713, v9
	v_mul_f32_e32 v5, v5, v9
	v_fmac_f32_e32 v11, v5, v11
	v_mul_f32_e32 v5, 0x3f4c422a, v11
	v_add_f32_e32 v5, v5, v5
	v_mul_f32_e32 v5, 0xbfb8aa3b, v5
	v_exp_f32_e32 v5, v5
	s_nop 0
	v_add_f32_e32 v5, 1.0, v5
	v_rcp_f32_e32 v11, v5
	s_nop 0
	v_pk_mul_f32 v[8:9], v[10:11], v[8:9]
	s_nop 0
	v_pk_mul_f32 v[6:7], v[8:9], v[6:7]
	s_nop 0
	v_cvt_pk_bf16_f32 v5, v6, v7
	v_mad_i64_i32 v[6:7], s[8:9], v0, s13, v[72:73]
	v_or_b32_e32 v0, s4, v81
	global_store_dwordx4 v[6:7], v[2:5], off
	v_mad_i64_i32 v[6:7], s[8:9], v0, s13, v[74:75]
	ds_read_b128 v[2:5], v110 offset:288
	s_waitcnt lgkmcnt(0)
	v_lshlrev_b32_e32 v10, 16, v2
	v_and_b32_e32 v11, 0xffff0000, v2
	s_waitcnt vmcnt(7)
	v_mov_b32_e32 v6, v24
	v_mov_b32_e32 v7, v25
	v_mov_b32_e32 v8, v26
	v_mov_b32_e32 v9, v27
	v_lshlrev_b32_e32 v12, 16, v6
	v_mul_f32_e32 v2, 0x3d372713, v12
	v_and_b32_e32 v13, 0xffff0000, v6
	v_mul_f32_e32 v2, v2, v12
	v_mov_b32_e32 v6, v12
	v_fmac_f32_e32 v6, v2, v6
	v_mul_f32_e32 v2, 0x3f4c422a, v6
	v_add_f32_e32 v2, v2, v2
	v_mul_f32_e32 v2, 0xbfb8aa3b, v2
	v_exp_f32_e32 v2, v2
	v_mov_b32_e32 v6, v13
	v_add_f32_e32 v2, 1.0, v2
	v_rcp_f32_e32 v14, v2
	v_mul_f32_e32 v2, 0x3d372713, v13
	v_mul_f32_e32 v2, v2, v13
	v_fmac_f32_e32 v6, v2, v6
	v_mul_f32_e32 v2, 0x3f4c422a, v6
	v_add_f32_e32 v2, v2, v2
	v_mul_f32_e32 v2, 0xbfb8aa3b, v2
	v_exp_f32_e32 v2, v2
	v_lshlrev_b32_e32 v6, 16, v7
	v_and_b32_e32 v7, 0xffff0000, v7
	v_add_f32_e32 v2, 1.0, v2
	v_rcp_f32_e32 v15, v2
	s_nop 0
	v_pk_mul_f32 v[12:13], v[14:15], v[12:13]
	s_nop 0
	v_pk_mul_f32 v[10:11], v[12:13], v[10:11]
	v_mov_b32_e32 v12, v6
	v_cvt_pk_bf16_f32 v2, v10, v11
	v_lshlrev_b32_e32 v10, 16, v3
	v_and_b32_e32 v11, 0xffff0000, v3
	v_mul_f32_e32 v3, 0x3d372713, v6
	v_mul_f32_e32 v3, v3, v6
	v_fmac_f32_e32 v12, v3, v12
	v_mul_f32_e32 v3, 0x3f4c422a, v12
	v_add_f32_e32 v3, v3, v3
	v_mul_f32_e32 v3, 0xbfb8aa3b, v3
	v_exp_f32_e32 v3, v3
	v_mov_b32_e32 v13, v7
	v_add_f32_e32 v3, 1.0, v3
	v_rcp_f32_e32 v12, v3
	v_mul_f32_e32 v3, 0x3d372713, v7
	v_mul_f32_e32 v3, v3, v7
	v_fmac_f32_e32 v13, v3, v13
	v_mul_f32_e32 v3, 0x3f4c422a, v13
	v_add_f32_e32 v3, v3, v3
	v_mul_f32_e32 v3, 0xbfb8aa3b, v3
	v_exp_f32_e32 v3, v3
	s_nop 0
	v_add_f32_e32 v3, 1.0, v3
	v_rcp_f32_e32 v13, v3
	s_nop 0
	v_pk_mul_f32 v[6:7], v[12:13], v[6:7]
	s_nop 0
	v_pk_mul_f32 v[6:7], v[6:7], v[10:11]
	v_lshlrev_b32_e32 v10, 16, v8
	v_cvt_pk_bf16_f32 v3, v6, v7
	v_lshlrev_b32_e32 v6, 16, v4
	v_and_b32_e32 v7, 0xffff0000, v4
	v_mul_f32_e32 v4, 0x3d372713, v10
	v_and_b32_e32 v11, 0xffff0000, v8
	v_mul_f32_e32 v4, v4, v10
	v_mov_b32_e32 v8, v10
	v_fmac_f32_e32 v8, v4, v8
	v_mul_f32_e32 v4, 0x3f4c422a, v8
	v_add_f32_e32 v4, v4, v4
	v_mul_f32_e32 v4, 0xbfb8aa3b, v4
	v_exp_f32_e32 v4, v4
	v_mov_b32_e32 v8, v11
	v_add_f32_e32 v4, 1.0, v4
	v_rcp_f32_e32 v12, v4
	v_mul_f32_e32 v4, 0x3d372713, v11
	v_mul_f32_e32 v4, v4, v11
	v_fmac_f32_e32 v8, v4, v8
	v_mul_f32_e32 v4, 0x3f4c422a, v8
	v_add_f32_e32 v4, v4, v4
	v_mul_f32_e32 v4, 0xbfb8aa3b, v4
	v_exp_f32_e32 v4, v4
	v_lshlrev_b32_e32 v8, 16, v9
	v_and_b32_e32 v9, 0xffff0000, v9
	v_add_f32_e32 v4, 1.0, v4
	v_rcp_f32_e32 v13, v4
	s_nop 0
	v_pk_mul_f32 v[10:11], v[12:13], v[10:11]
	s_nop 0
	v_pk_mul_f32 v[6:7], v[10:11], v[6:7]
	v_mov_b32_e32 v10, v8
	v_cvt_pk_bf16_f32 v4, v6, v7
	v_lshlrev_b32_e32 v6, 16, v5
	v_and_b32_e32 v7, 0xffff0000, v5
	v_mul_f32_e32 v5, 0x3d372713, v8
	v_mul_f32_e32 v5, v5, v8
	v_fmac_f32_e32 v10, v5, v10
	v_mul_f32_e32 v5, 0x3f4c422a, v10
	v_add_f32_e32 v5, v5, v5
	v_mul_f32_e32 v5, 0xbfb8aa3b, v5
	v_exp_f32_e32 v5, v5
	v_mov_b32_e32 v11, v9
	v_add_f32_e32 v5, 1.0, v5
	v_rcp_f32_e32 v10, v5
	v_mul_f32_e32 v5, 0x3d372713, v9
	v_mul_f32_e32 v5, v5, v9
	v_fmac_f32_e32 v11, v5, v11
	v_mul_f32_e32 v5, 0x3f4c422a, v11
	v_add_f32_e32 v5, v5, v5
	v_mul_f32_e32 v5, 0xbfb8aa3b, v5
	v_exp_f32_e32 v5, v5
	s_nop 0
	v_add_f32_e32 v5, 1.0, v5
	v_rcp_f32_e32 v11, v5
	s_nop 0
	v_pk_mul_f32 v[8:9], v[10:11], v[8:9]
	s_nop 0
	v_pk_mul_f32 v[6:7], v[8:9], v[6:7]
	s_nop 0
	v_cvt_pk_bf16_f32 v5, v6, v7
	v_mad_i64_i32 v[6:7], s[8:9], v0, s13, v[72:73]
	v_or_b32_e32 v0, s4, v83
	global_store_dwordx4 v[6:7], v[2:5], off
	v_mad_i64_i32 v[6:7], s[8:9], v0, s13, v[74:75]
	ds_read_b128 v[2:5], v111 offset:288
	s_waitcnt lgkmcnt(0)
	v_lshlrev_b32_e32 v10, 16, v2
	v_and_b32_e32 v11, 0xffff0000, v2
	s_waitcnt vmcnt(7)
	v_mov_b32_e32 v6, v28
	v_mov_b32_e32 v7, v29
	v_mov_b32_e32 v8, v30
	v_mov_b32_e32 v9, v31
	v_lshlrev_b32_e32 v12, 16, v6
	v_mul_f32_e32 v2, 0x3d372713, v12
	v_and_b32_e32 v13, 0xffff0000, v6
	v_mul_f32_e32 v2, v2, v12
	v_mov_b32_e32 v6, v12
	v_fmac_f32_e32 v6, v2, v6
	v_mul_f32_e32 v2, 0x3f4c422a, v6
	v_add_f32_e32 v2, v2, v2
	v_mul_f32_e32 v2, 0xbfb8aa3b, v2
	v_exp_f32_e32 v2, v2
	v_mov_b32_e32 v6, v13
	v_add_f32_e32 v2, 1.0, v2
	v_rcp_f32_e32 v14, v2
	v_mul_f32_e32 v2, 0x3d372713, v13
	v_mul_f32_e32 v2, v2, v13
	v_fmac_f32_e32 v6, v2, v6
	v_mul_f32_e32 v2, 0x3f4c422a, v6
	v_add_f32_e32 v2, v2, v2
	v_mul_f32_e32 v2, 0xbfb8aa3b, v2
	v_exp_f32_e32 v2, v2
	v_lshlrev_b32_e32 v6, 16, v7
	v_and_b32_e32 v7, 0xffff0000, v7
	v_add_f32_e32 v2, 1.0, v2
	v_rcp_f32_e32 v15, v2
	s_nop 0
	v_pk_mul_f32 v[12:13], v[14:15], v[12:13]
	s_nop 0
	v_pk_mul_f32 v[10:11], v[12:13], v[10:11]
	v_mov_b32_e32 v12, v6
	v_cvt_pk_bf16_f32 v2, v10, v11
	v_lshlrev_b32_e32 v10, 16, v3
	v_and_b32_e32 v11, 0xffff0000, v3
	v_mul_f32_e32 v3, 0x3d372713, v6
	v_mul_f32_e32 v3, v3, v6
	v_fmac_f32_e32 v12, v3, v12
	v_mul_f32_e32 v3, 0x3f4c422a, v12
	v_add_f32_e32 v3, v3, v3
	v_mul_f32_e32 v3, 0xbfb8aa3b, v3
	v_exp_f32_e32 v3, v3
	v_mov_b32_e32 v13, v7
	v_add_f32_e32 v3, 1.0, v3
	v_rcp_f32_e32 v12, v3
	v_mul_f32_e32 v3, 0x3d372713, v7
	v_mul_f32_e32 v3, v3, v7
	v_fmac_f32_e32 v13, v3, v13
	v_mul_f32_e32 v3, 0x3f4c422a, v13
	v_add_f32_e32 v3, v3, v3
	v_mul_f32_e32 v3, 0xbfb8aa3b, v3
	v_exp_f32_e32 v3, v3
	s_nop 0
	v_add_f32_e32 v3, 1.0, v3
	v_rcp_f32_e32 v13, v3
	s_nop 0
	v_pk_mul_f32 v[6:7], v[12:13], v[6:7]
	s_nop 0
	v_pk_mul_f32 v[6:7], v[6:7], v[10:11]
	v_lshlrev_b32_e32 v10, 16, v8
	v_cvt_pk_bf16_f32 v3, v6, v7
	v_lshlrev_b32_e32 v6, 16, v4
	v_and_b32_e32 v7, 0xffff0000, v4
	v_mul_f32_e32 v4, 0x3d372713, v10
	v_and_b32_e32 v11, 0xffff0000, v8
	v_mul_f32_e32 v4, v4, v10
	v_mov_b32_e32 v8, v10
	v_fmac_f32_e32 v8, v4, v8
	v_mul_f32_e32 v4, 0x3f4c422a, v8
	v_add_f32_e32 v4, v4, v4
	v_mul_f32_e32 v4, 0xbfb8aa3b, v4
	v_exp_f32_e32 v4, v4
	v_mov_b32_e32 v8, v11
	v_add_f32_e32 v4, 1.0, v4
	v_rcp_f32_e32 v12, v4
	v_mul_f32_e32 v4, 0x3d372713, v11
	v_mul_f32_e32 v4, v4, v11
	v_fmac_f32_e32 v8, v4, v8
	v_mul_f32_e32 v4, 0x3f4c422a, v8
	v_add_f32_e32 v4, v4, v4
	v_mul_f32_e32 v4, 0xbfb8aa3b, v4
	v_exp_f32_e32 v4, v4
	v_lshlrev_b32_e32 v8, 16, v9
	v_and_b32_e32 v9, 0xffff0000, v9
	v_add_f32_e32 v4, 1.0, v4
	v_rcp_f32_e32 v13, v4
	s_nop 0
	v_pk_mul_f32 v[10:11], v[12:13], v[10:11]
	s_nop 0
	v_pk_mul_f32 v[6:7], v[10:11], v[6:7]
	v_mov_b32_e32 v10, v8
	v_cvt_pk_bf16_f32 v4, v6, v7
	v_lshlrev_b32_e32 v6, 16, v5
	v_and_b32_e32 v7, 0xffff0000, v5
	v_mul_f32_e32 v5, 0x3d372713, v8
	v_mul_f32_e32 v5, v5, v8
	v_fmac_f32_e32 v10, v5, v10
	v_mul_f32_e32 v5, 0x3f4c422a, v10
	v_add_f32_e32 v5, v5, v5
	v_mul_f32_e32 v5, 0xbfb8aa3b, v5
	v_exp_f32_e32 v5, v5
	v_mov_b32_e32 v11, v9
	v_add_f32_e32 v5, 1.0, v5
	v_rcp_f32_e32 v10, v5
	v_mul_f32_e32 v5, 0x3d372713, v9
	v_mul_f32_e32 v5, v5, v9
	v_fmac_f32_e32 v11, v5, v11
	v_mul_f32_e32 v5, 0x3f4c422a, v11
	v_add_f32_e32 v5, v5, v5
	v_mul_f32_e32 v5, 0xbfb8aa3b, v5
	v_exp_f32_e32 v5, v5
	s_nop 0
	v_add_f32_e32 v5, 1.0, v5
	v_rcp_f32_e32 v11, v5
	s_nop 0
	v_pk_mul_f32 v[8:9], v[10:11], v[8:9]
	s_nop 0
	v_pk_mul_f32 v[6:7], v[8:9], v[6:7]
	s_nop 0
	v_cvt_pk_bf16_f32 v5, v6, v7
	v_mad_i64_i32 v[6:7], s[8:9], v0, s13, v[72:73]
	v_or_b32_e32 v0, s4, v85
	global_store_dwordx4 v[6:7], v[2:5], off
	v_mad_i64_i32 v[6:7], s[8:9], v0, s13, v[74:75]
	ds_read_b128 v[2:5], v112 offset:288
	s_waitcnt lgkmcnt(0)
	v_lshlrev_b32_e32 v10, 16, v2
	v_and_b32_e32 v11, 0xffff0000, v2
	s_waitcnt vmcnt(7)
	v_mov_b32_e32 v6, v32
	v_mov_b32_e32 v7, v33
	v_mov_b32_e32 v8, v34
	v_mov_b32_e32 v9, v35
	v_lshlrev_b32_e32 v12, 16, v6
	v_mul_f32_e32 v2, 0x3d372713, v12
	v_and_b32_e32 v13, 0xffff0000, v6
	v_mul_f32_e32 v2, v2, v12
	v_mov_b32_e32 v6, v12
	v_fmac_f32_e32 v6, v2, v6
	v_mul_f32_e32 v2, 0x3f4c422a, v6
	v_add_f32_e32 v2, v2, v2
	v_mul_f32_e32 v2, 0xbfb8aa3b, v2
	v_exp_f32_e32 v2, v2
	v_mov_b32_e32 v6, v13
	v_add_f32_e32 v2, 1.0, v2
	v_rcp_f32_e32 v14, v2
	v_mul_f32_e32 v2, 0x3d372713, v13
	v_mul_f32_e32 v2, v2, v13
	v_fmac_f32_e32 v6, v2, v6
	v_mul_f32_e32 v2, 0x3f4c422a, v6
	v_add_f32_e32 v2, v2, v2
	v_mul_f32_e32 v2, 0xbfb8aa3b, v2
	v_exp_f32_e32 v2, v2
	v_lshlrev_b32_e32 v6, 16, v7
	v_and_b32_e32 v7, 0xffff0000, v7
	v_add_f32_e32 v2, 1.0, v2
	v_rcp_f32_e32 v15, v2
	s_nop 0
	v_pk_mul_f32 v[12:13], v[14:15], v[12:13]
	s_nop 0
	v_pk_mul_f32 v[10:11], v[12:13], v[10:11]
	v_mov_b32_e32 v12, v6
	v_cvt_pk_bf16_f32 v2, v10, v11
	v_lshlrev_b32_e32 v10, 16, v3
	v_and_b32_e32 v11, 0xffff0000, v3
	v_mul_f32_e32 v3, 0x3d372713, v6
	v_mul_f32_e32 v3, v3, v6
	v_fmac_f32_e32 v12, v3, v12
	v_mul_f32_e32 v3, 0x3f4c422a, v12
	v_add_f32_e32 v3, v3, v3
	v_mul_f32_e32 v3, 0xbfb8aa3b, v3
	v_exp_f32_e32 v3, v3
	v_mov_b32_e32 v13, v7
	v_add_f32_e32 v3, 1.0, v3
	v_rcp_f32_e32 v12, v3
	v_mul_f32_e32 v3, 0x3d372713, v7
	v_mul_f32_e32 v3, v3, v7
	v_fmac_f32_e32 v13, v3, v13
	v_mul_f32_e32 v3, 0x3f4c422a, v13
	v_add_f32_e32 v3, v3, v3
	v_mul_f32_e32 v3, 0xbfb8aa3b, v3
	v_exp_f32_e32 v3, v3
	s_nop 0
	v_add_f32_e32 v3, 1.0, v3
	v_rcp_f32_e32 v13, v3
	s_nop 0
	v_pk_mul_f32 v[6:7], v[12:13], v[6:7]
	s_nop 0
	v_pk_mul_f32 v[6:7], v[6:7], v[10:11]
	v_lshlrev_b32_e32 v10, 16, v8
	v_cvt_pk_bf16_f32 v3, v6, v7
	v_lshlrev_b32_e32 v6, 16, v4
	v_and_b32_e32 v7, 0xffff0000, v4
	v_mul_f32_e32 v4, 0x3d372713, v10
	v_and_b32_e32 v11, 0xffff0000, v8
	v_mul_f32_e32 v4, v4, v10
	v_mov_b32_e32 v8, v10
	v_fmac_f32_e32 v8, v4, v8
	v_mul_f32_e32 v4, 0x3f4c422a, v8
	v_add_f32_e32 v4, v4, v4
	v_mul_f32_e32 v4, 0xbfb8aa3b, v4
	v_exp_f32_e32 v4, v4
	v_mov_b32_e32 v8, v11
	v_add_f32_e32 v4, 1.0, v4
	v_rcp_f32_e32 v12, v4
	v_mul_f32_e32 v4, 0x3d372713, v11
	v_mul_f32_e32 v4, v4, v11
	v_fmac_f32_e32 v8, v4, v8
	v_mul_f32_e32 v4, 0x3f4c422a, v8
	v_add_f32_e32 v4, v4, v4
	v_mul_f32_e32 v4, 0xbfb8aa3b, v4
	v_exp_f32_e32 v4, v4
	v_lshlrev_b32_e32 v8, 16, v9
	v_and_b32_e32 v9, 0xffff0000, v9
	v_add_f32_e32 v4, 1.0, v4
	v_rcp_f32_e32 v13, v4
	s_nop 0
	v_pk_mul_f32 v[10:11], v[12:13], v[10:11]
	s_nop 0
	v_pk_mul_f32 v[6:7], v[10:11], v[6:7]
	v_mov_b32_e32 v10, v8
	v_cvt_pk_bf16_f32 v4, v6, v7
	v_lshlrev_b32_e32 v6, 16, v5
	v_and_b32_e32 v7, 0xffff0000, v5
	v_mul_f32_e32 v5, 0x3d372713, v8
	v_mul_f32_e32 v5, v5, v8
	v_fmac_f32_e32 v10, v5, v10
	v_mul_f32_e32 v5, 0x3f4c422a, v10
	v_add_f32_e32 v5, v5, v5
	v_mul_f32_e32 v5, 0xbfb8aa3b, v5
	v_exp_f32_e32 v5, v5
	v_mov_b32_e32 v11, v9
	v_add_f32_e32 v5, 1.0, v5
	v_rcp_f32_e32 v10, v5
	v_mul_f32_e32 v5, 0x3d372713, v9
	v_mul_f32_e32 v5, v5, v9
	v_fmac_f32_e32 v11, v5, v11
	v_mul_f32_e32 v5, 0x3f4c422a, v11
	v_add_f32_e32 v5, v5, v5
	v_mul_f32_e32 v5, 0xbfb8aa3b, v5
	v_exp_f32_e32 v5, v5
	s_nop 0
	v_add_f32_e32 v5, 1.0, v5
	v_rcp_f32_e32 v11, v5
	s_nop 0
	v_pk_mul_f32 v[8:9], v[10:11], v[8:9]
	s_nop 0
	v_pk_mul_f32 v[6:7], v[8:9], v[6:7]
	s_nop 0
	v_cvt_pk_bf16_f32 v5, v6, v7
	v_mad_i64_i32 v[6:7], s[8:9], v0, s13, v[72:73]
	v_or_b32_e32 v0, s4, v87
	global_store_dwordx4 v[6:7], v[2:5], off
	v_mad_i64_i32 v[6:7], s[8:9], v0, s13, v[74:75]
	ds_read_b128 v[2:5], v113 offset:288
	s_waitcnt lgkmcnt(0)
	v_lshlrev_b32_e32 v10, 16, v2
	v_and_b32_e32 v11, 0xffff0000, v2
	s_waitcnt vmcnt(7)
	v_mov_b32_e32 v6, v36
	v_mov_b32_e32 v7, v37
	v_mov_b32_e32 v8, v38
	v_mov_b32_e32 v9, v39
	v_lshlrev_b32_e32 v12, 16, v6
	v_mul_f32_e32 v2, 0x3d372713, v12
	v_and_b32_e32 v13, 0xffff0000, v6
	v_mul_f32_e32 v2, v2, v12
	v_mov_b32_e32 v6, v12
	v_fmac_f32_e32 v6, v2, v6
	v_mul_f32_e32 v2, 0x3f4c422a, v6
	v_add_f32_e32 v2, v2, v2
	v_mul_f32_e32 v2, 0xbfb8aa3b, v2
	v_exp_f32_e32 v2, v2
	v_mov_b32_e32 v6, v13
	v_add_f32_e32 v2, 1.0, v2
	v_rcp_f32_e32 v14, v2
	v_mul_f32_e32 v2, 0x3d372713, v13
	v_mul_f32_e32 v2, v2, v13
	v_fmac_f32_e32 v6, v2, v6
	v_mul_f32_e32 v2, 0x3f4c422a, v6
	v_add_f32_e32 v2, v2, v2
	v_mul_f32_e32 v2, 0xbfb8aa3b, v2
	v_exp_f32_e32 v2, v2
	v_lshlrev_b32_e32 v6, 16, v7
	v_and_b32_e32 v7, 0xffff0000, v7
	v_add_f32_e32 v2, 1.0, v2
	v_rcp_f32_e32 v15, v2
	s_nop 0
	v_pk_mul_f32 v[12:13], v[14:15], v[12:13]
	s_nop 0
	v_pk_mul_f32 v[10:11], v[12:13], v[10:11]
	v_mov_b32_e32 v12, v6
	v_cvt_pk_bf16_f32 v2, v10, v11
	v_lshlrev_b32_e32 v10, 16, v3
	v_and_b32_e32 v11, 0xffff0000, v3
	v_mul_f32_e32 v3, 0x3d372713, v6
	v_mul_f32_e32 v3, v3, v6
	v_fmac_f32_e32 v12, v3, v12
	v_mul_f32_e32 v3, 0x3f4c422a, v12
	v_add_f32_e32 v3, v3, v3
	v_mul_f32_e32 v3, 0xbfb8aa3b, v3
	v_exp_f32_e32 v3, v3
	v_mov_b32_e32 v13, v7
	v_add_f32_e32 v3, 1.0, v3
	v_rcp_f32_e32 v12, v3
	v_mul_f32_e32 v3, 0x3d372713, v7
	v_mul_f32_e32 v3, v3, v7
	v_fmac_f32_e32 v13, v3, v13
	v_mul_f32_e32 v3, 0x3f4c422a, v13
	v_add_f32_e32 v3, v3, v3
	v_mul_f32_e32 v3, 0xbfb8aa3b, v3
	v_exp_f32_e32 v3, v3
	s_nop 0
	v_add_f32_e32 v3, 1.0, v3
	v_rcp_f32_e32 v13, v3
	s_nop 0
	v_pk_mul_f32 v[6:7], v[12:13], v[6:7]
	s_nop 0
	v_pk_mul_f32 v[6:7], v[6:7], v[10:11]
	v_lshlrev_b32_e32 v10, 16, v8
	v_cvt_pk_bf16_f32 v3, v6, v7
	v_lshlrev_b32_e32 v6, 16, v4
	v_and_b32_e32 v7, 0xffff0000, v4
	v_mul_f32_e32 v4, 0x3d372713, v10
	v_and_b32_e32 v11, 0xffff0000, v8
	v_mul_f32_e32 v4, v4, v10
	v_mov_b32_e32 v8, v10
	v_fmac_f32_e32 v8, v4, v8
	v_mul_f32_e32 v4, 0x3f4c422a, v8
	v_add_f32_e32 v4, v4, v4
	v_mul_f32_e32 v4, 0xbfb8aa3b, v4
	v_exp_f32_e32 v4, v4
	v_mov_b32_e32 v8, v11
	v_add_f32_e32 v4, 1.0, v4
	v_rcp_f32_e32 v12, v4
	v_mul_f32_e32 v4, 0x3d372713, v11
	v_mul_f32_e32 v4, v4, v11
	v_fmac_f32_e32 v8, v4, v8
	v_mul_f32_e32 v4, 0x3f4c422a, v8
	v_add_f32_e32 v4, v4, v4
	v_mul_f32_e32 v4, 0xbfb8aa3b, v4
	v_exp_f32_e32 v4, v4
	v_lshlrev_b32_e32 v8, 16, v9
	v_and_b32_e32 v9, 0xffff0000, v9
	v_add_f32_e32 v4, 1.0, v4
	v_rcp_f32_e32 v13, v4
	s_nop 0
	v_pk_mul_f32 v[10:11], v[12:13], v[10:11]
	s_nop 0
	v_pk_mul_f32 v[6:7], v[10:11], v[6:7]
	v_mov_b32_e32 v10, v8
	v_cvt_pk_bf16_f32 v4, v6, v7
	v_lshlrev_b32_e32 v6, 16, v5
	v_and_b32_e32 v7, 0xffff0000, v5
	v_mul_f32_e32 v5, 0x3d372713, v8
	v_mul_f32_e32 v5, v5, v8
	v_fmac_f32_e32 v10, v5, v10
	v_mul_f32_e32 v5, 0x3f4c422a, v10
	v_add_f32_e32 v5, v5, v5
	v_mul_f32_e32 v5, 0xbfb8aa3b, v5
	v_exp_f32_e32 v5, v5
	v_mov_b32_e32 v11, v9
	v_add_f32_e32 v5, 1.0, v5
	v_rcp_f32_e32 v10, v5
	v_mul_f32_e32 v5, 0x3d372713, v9
	v_mul_f32_e32 v5, v5, v9
	v_fmac_f32_e32 v11, v5, v11
	v_mul_f32_e32 v5, 0x3f4c422a, v11
	v_add_f32_e32 v5, v5, v5
	v_mul_f32_e32 v5, 0xbfb8aa3b, v5
	v_exp_f32_e32 v5, v5
	s_nop 0
	v_add_f32_e32 v5, 1.0, v5
	v_rcp_f32_e32 v11, v5
	s_nop 0
	v_pk_mul_f32 v[8:9], v[10:11], v[8:9]
	s_nop 0
	v_pk_mul_f32 v[6:7], v[8:9], v[6:7]
	s_nop 0
	v_cvt_pk_bf16_f32 v5, v6, v7
	v_mad_i64_i32 v[6:7], s[8:9], v0, s13, v[72:73]
	v_or_b32_e32 v0, s4, v89
	global_store_dwordx4 v[6:7], v[2:5], off
	v_mad_i64_i32 v[6:7], s[8:9], v0, s13, v[74:75]
	ds_read_b128 v[2:5], v114 offset:288
	s_waitcnt lgkmcnt(0)
	v_lshlrev_b32_e32 v10, 16, v2
	v_and_b32_e32 v11, 0xffff0000, v2
	s_waitcnt vmcnt(7)
	v_mov_b32_e32 v6, v40
	v_mov_b32_e32 v7, v41
	v_mov_b32_e32 v8, v42
	v_mov_b32_e32 v9, v43
	v_lshlrev_b32_e32 v12, 16, v6
	v_mul_f32_e32 v2, 0x3d372713, v12
	v_and_b32_e32 v13, 0xffff0000, v6
	v_mul_f32_e32 v2, v2, v12
	v_mov_b32_e32 v6, v12
	v_fmac_f32_e32 v6, v2, v6
	v_mul_f32_e32 v2, 0x3f4c422a, v6
	v_add_f32_e32 v2, v2, v2
	v_mul_f32_e32 v2, 0xbfb8aa3b, v2
	v_exp_f32_e32 v2, v2
	v_mov_b32_e32 v6, v13
	v_add_f32_e32 v2, 1.0, v2
	v_rcp_f32_e32 v14, v2
	v_mul_f32_e32 v2, 0x3d372713, v13
	v_mul_f32_e32 v2, v2, v13
	v_fmac_f32_e32 v6, v2, v6
	v_mul_f32_e32 v2, 0x3f4c422a, v6
	v_add_f32_e32 v2, v2, v2
	v_mul_f32_e32 v2, 0xbfb8aa3b, v2
	v_exp_f32_e32 v2, v2
	v_lshlrev_b32_e32 v6, 16, v7
	v_and_b32_e32 v7, 0xffff0000, v7
	v_add_f32_e32 v2, 1.0, v2
	v_rcp_f32_e32 v15, v2
	s_nop 0
	v_pk_mul_f32 v[12:13], v[14:15], v[12:13]
	s_nop 0
	v_pk_mul_f32 v[10:11], v[12:13], v[10:11]
	v_mov_b32_e32 v12, v6
	v_cvt_pk_bf16_f32 v2, v10, v11
	v_lshlrev_b32_e32 v10, 16, v3
	v_and_b32_e32 v11, 0xffff0000, v3
	v_mul_f32_e32 v3, 0x3d372713, v6
	v_mul_f32_e32 v3, v3, v6
	v_fmac_f32_e32 v12, v3, v12
	v_mul_f32_e32 v3, 0x3f4c422a, v12
	v_add_f32_e32 v3, v3, v3
	v_mul_f32_e32 v3, 0xbfb8aa3b, v3
	v_exp_f32_e32 v3, v3
	v_mov_b32_e32 v13, v7
	v_add_f32_e32 v3, 1.0, v3
	v_rcp_f32_e32 v12, v3
	v_mul_f32_e32 v3, 0x3d372713, v7
	v_mul_f32_e32 v3, v3, v7
	v_fmac_f32_e32 v13, v3, v13
	v_mul_f32_e32 v3, 0x3f4c422a, v13
	v_add_f32_e32 v3, v3, v3
	v_mul_f32_e32 v3, 0xbfb8aa3b, v3
	v_exp_f32_e32 v3, v3
	s_nop 0
	v_add_f32_e32 v3, 1.0, v3
	v_rcp_f32_e32 v13, v3
	s_nop 0
	v_pk_mul_f32 v[6:7], v[12:13], v[6:7]
	s_nop 0
	v_pk_mul_f32 v[6:7], v[6:7], v[10:11]
	v_lshlrev_b32_e32 v10, 16, v8
	v_cvt_pk_bf16_f32 v3, v6, v7
	v_lshlrev_b32_e32 v6, 16, v4
	v_and_b32_e32 v7, 0xffff0000, v4
	v_mul_f32_e32 v4, 0x3d372713, v10
	v_and_b32_e32 v11, 0xffff0000, v8
	v_mul_f32_e32 v4, v4, v10
	v_mov_b32_e32 v8, v10
	v_fmac_f32_e32 v8, v4, v8
	v_mul_f32_e32 v4, 0x3f4c422a, v8
	v_add_f32_e32 v4, v4, v4
	v_mul_f32_e32 v4, 0xbfb8aa3b, v4
	v_exp_f32_e32 v4, v4
	v_mov_b32_e32 v8, v11
	v_add_f32_e32 v4, 1.0, v4
	v_rcp_f32_e32 v12, v4
	v_mul_f32_e32 v4, 0x3d372713, v11
	v_mul_f32_e32 v4, v4, v11
	v_fmac_f32_e32 v8, v4, v8
	v_mul_f32_e32 v4, 0x3f4c422a, v8
	v_add_f32_e32 v4, v4, v4
	v_mul_f32_e32 v4, 0xbfb8aa3b, v4
	v_exp_f32_e32 v4, v4
	v_lshlrev_b32_e32 v8, 16, v9
	v_and_b32_e32 v9, 0xffff0000, v9
	v_add_f32_e32 v4, 1.0, v4
	v_rcp_f32_e32 v13, v4
	s_nop 0
	v_pk_mul_f32 v[10:11], v[12:13], v[10:11]
	s_nop 0
	v_pk_mul_f32 v[6:7], v[10:11], v[6:7]
	v_mov_b32_e32 v10, v8
	v_cvt_pk_bf16_f32 v4, v6, v7
	v_lshlrev_b32_e32 v6, 16, v5
	v_and_b32_e32 v7, 0xffff0000, v5
	v_mul_f32_e32 v5, 0x3d372713, v8
	v_mul_f32_e32 v5, v5, v8
	v_fmac_f32_e32 v10, v5, v10
	v_mul_f32_e32 v5, 0x3f4c422a, v10
	v_add_f32_e32 v5, v5, v5
	v_mul_f32_e32 v5, 0xbfb8aa3b, v5
	v_exp_f32_e32 v5, v5
	v_mov_b32_e32 v11, v9
	v_add_f32_e32 v5, 1.0, v5
	v_rcp_f32_e32 v10, v5
	v_mul_f32_e32 v5, 0x3d372713, v9
	v_mul_f32_e32 v5, v5, v9
	v_fmac_f32_e32 v11, v5, v11
	v_mul_f32_e32 v5, 0x3f4c422a, v11
	v_add_f32_e32 v5, v5, v5
	v_mul_f32_e32 v5, 0xbfb8aa3b, v5
	v_exp_f32_e32 v5, v5
	s_nop 0
	v_add_f32_e32 v5, 1.0, v5
	v_rcp_f32_e32 v11, v5
	s_nop 0
	v_pk_mul_f32 v[8:9], v[10:11], v[8:9]
	s_nop 0
	v_pk_mul_f32 v[6:7], v[8:9], v[6:7]
	s_nop 0
	v_cvt_pk_bf16_f32 v5, v6, v7
	v_mad_i64_i32 v[6:7], s[8:9], v0, s13, v[72:73]
	v_or_b32_e32 v0, s4, v91
	global_store_dwordx4 v[6:7], v[2:5], off
	ds_read_b128 v[6:9], v115 offset:288
	s_waitcnt lgkmcnt(0)
	v_lshlrev_b32_e32 v10, 16, v6
	v_mad_i64_i32 v[2:3], s[4:5], v0, s13, v[74:75]
	v_and_b32_e32 v11, 0xffff0000, v6
	s_waitcnt vmcnt(7)
	v_mov_b32_e32 v2, v44
	v_mov_b32_e32 v3, v45
	v_mov_b32_e32 v4, v46
	v_mov_b32_e32 v5, v47
	v_lshlrev_b32_e32 v12, 16, v2
	v_and_b32_e32 v13, 0xffff0000, v2
	v_mul_f32_e32 v2, 0x3d372713, v12
	v_mul_f32_e32 v2, v2, v12
	v_mov_b32_e32 v6, v12
	v_fmac_f32_e32 v6, v2, v6
	v_mul_f32_e32 v2, 0x3f4c422a, v6
	v_add_f32_e32 v2, v2, v2
	v_mul_f32_e32 v2, 0xbfb8aa3b, v2
	v_exp_f32_e32 v2, v2
	v_mov_b32_e32 v6, v13
	v_add_f32_e32 v2, 1.0, v2
	v_rcp_f32_e32 v14, v2
	v_mul_f32_e32 v2, 0x3d372713, v13
	v_mul_f32_e32 v2, v2, v13
	v_fmac_f32_e32 v6, v2, v6
	v_mul_f32_e32 v2, 0x3f4c422a, v6
	v_add_f32_e32 v2, v2, v2
	v_mul_f32_e32 v2, 0xbfb8aa3b, v2
	v_exp_f32_e32 v2, v2
	v_lshlrev_b32_e32 v6, 16, v7
	v_and_b32_e32 v7, 0xffff0000, v7
	v_add_f32_e32 v2, 1.0, v2
	v_rcp_f32_e32 v15, v2
	s_nop 0
	v_pk_mul_f32 v[12:13], v[14:15], v[12:13]
	s_nop 0
	v_pk_mul_f32 v[10:11], v[12:13], v[10:11]
	s_nop 0
	v_cvt_pk_bf16_f32 v2, v10, v11
	v_lshlrev_b32_e32 v10, 16, v3
	v_and_b32_e32 v11, 0xffff0000, v3
	v_mul_f32_e32 v3, 0x3d372713, v10
	v_mul_f32_e32 v3, v3, v10
	v_mov_b32_e32 v12, v10
	v_fmac_f32_e32 v12, v3, v12
	v_mul_f32_e32 v3, 0x3f4c422a, v12
	v_add_f32_e32 v3, v3, v3
	v_mul_f32_e32 v3, 0xbfb8aa3b, v3
	v_exp_f32_e32 v3, v3
	v_mov_b32_e32 v13, v11
	v_add_f32_e32 v3, 1.0, v3
	v_rcp_f32_e32 v12, v3
	v_mul_f32_e32 v3, 0x3d372713, v11
	v_mul_f32_e32 v3, v3, v11
	v_fmac_f32_e32 v13, v3, v13
	v_mul_f32_e32 v3, 0x3f4c422a, v13
	v_add_f32_e32 v3, v3, v3
	v_mul_f32_e32 v3, 0xbfb8aa3b, v3
	v_exp_f32_e32 v3, v3
	s_nop 0
	v_add_f32_e32 v3, 1.0, v3
	v_rcp_f32_e32 v13, v3
	s_nop 0
	v_pk_mul_f32 v[10:11], v[12:13], v[10:11]
	s_nop 0
	v_pk_mul_f32 v[6:7], v[10:11], v[6:7]
	v_lshlrev_b32_e32 v10, 16, v4
	v_and_b32_e32 v11, 0xffff0000, v4
	v_mul_f32_e32 v4, 0x3d372713, v10
	v_cvt_pk_bf16_f32 v3, v6, v7
	v_lshlrev_b32_e32 v6, 16, v8
	v_and_b32_e32 v7, 0xffff0000, v8
	v_mul_f32_e32 v4, v4, v10
	v_mov_b32_e32 v8, v10
	v_fmac_f32_e32 v8, v4, v8
	v_mul_f32_e32 v4, 0x3f4c422a, v8
	v_add_f32_e32 v4, v4, v4
	v_mul_f32_e32 v4, 0xbfb8aa3b, v4
	v_exp_f32_e32 v4, v4
	v_mov_b32_e32 v8, v11
	v_add_f32_e32 v4, 1.0, v4
	v_rcp_f32_e32 v12, v4
	v_mul_f32_e32 v4, 0x3d372713, v11
	v_mul_f32_e32 v4, v4, v11
	v_fmac_f32_e32 v8, v4, v8
	v_mul_f32_e32 v4, 0x3f4c422a, v8
	v_add_f32_e32 v4, v4, v4
	v_mul_f32_e32 v4, 0xbfb8aa3b, v4
	v_exp_f32_e32 v4, v4
	v_lshlrev_b32_e32 v8, 16, v5
	v_add_f32_e32 v4, 1.0, v4
	v_rcp_f32_e32 v13, v4
	s_nop 0
	v_pk_mul_f32 v[10:11], v[12:13], v[10:11]
	s_nop 0
	v_pk_mul_f32 v[6:7], v[10:11], v[6:7]
	v_mov_b32_e32 v10, v8
	v_cvt_pk_bf16_f32 v4, v6, v7
	v_lshlrev_b32_e32 v6, 16, v9
	v_and_b32_e32 v7, 0xffff0000, v9
	v_and_b32_e32 v9, 0xffff0000, v5
	v_mul_f32_e32 v5, 0x3d372713, v8
	v_mul_f32_e32 v5, v5, v8
	v_fmac_f32_e32 v10, v5, v10
	v_mul_f32_e32 v5, 0x3f4c422a, v10
	v_add_f32_e32 v5, v5, v5
	v_mul_f32_e32 v5, 0xbfb8aa3b, v5
	v_exp_f32_e32 v5, v5
	v_mov_b32_e32 v11, v9
	v_add_f32_e32 v5, 1.0, v5
	v_rcp_f32_e32 v10, v5
	v_mul_f32_e32 v5, 0x3d372713, v9
	v_mul_f32_e32 v5, v5, v9
	v_fmac_f32_e32 v11, v5, v11
	v_mul_f32_e32 v5, 0x3f4c422a, v11
	v_add_f32_e32 v5, v5, v5
	v_mul_f32_e32 v5, 0xbfb8aa3b, v5
	v_exp_f32_e32 v5, v5
	s_nop 0
	v_add_f32_e32 v5, 1.0, v5
	v_rcp_f32_e32 v11, v5
	s_nop 0
	v_pk_mul_f32 v[8:9], v[10:11], v[8:9]
	s_nop 0
	v_pk_mul_f32 v[6:7], v[8:9], v[6:7]
	s_nop 0
	v_cvt_pk_bf16_f32 v5, v6, v7
	v_mad_i64_i32 v[6:7], s[4:5], v0, s13, v[72:73]
	global_store_dwordx4 v[6:7], v[2:5], off
	s_waitcnt lgkmcnt(0)
	s_cbranch_scc1 .LBB0_600
	v_readlane_b32 s44, v253, 43
	v_readlane_b32 s45, v253, 44
	s_movk_i32 s43, 0x4000
	v_readlane_b32 s47, v253, 50
